# exp_v token loop software-pipelined across tokens: next token's 16 gathers issued into a second register set after the 4th gather of the current token is consumed (loop unrolled by two)
# speedup vs baseline: 1.0080x; 1.0080x over previous
; #define EV_LOADN(q_, g0_, n_) _Pragma("unroll") for (int k = 0; k < (n_); ++k) q_[k] = __builtin_bit_cast(uint4, __builtin_amdgcn_raw_buffer_load_b128(vrs, voff + si[((g0_) + k) * 8 + sub] * 128, 0, GATHER_AUX))
; __device__ void phase_exp_v(KParams& p, char* smem) {
;     ...
;       const int chunk = sh[0];
;       const unsigned x = (unsigned)sh[1];
;       if (chunk < 0) break;
;       int e0n = p.idx[(size_t)(chunk * 64 + w * 16) * 128 + lane], e1n = p.idx[(size_t)(chunk * 64 + w * 16) * 128 + 64 + lane];
;       float g0n = p.gate[(size_t)(chunk * 64 + w * 16) * 128 + lane], g1n = p.gate[(size_t)(chunk * 64 + w * 16) * 128 + 64 + lane];
;       for (int tt = 0; tt < 16; ++tt) {
;         const int t = chunk * 64 + w * 16 + tt;
;         __builtin_amdgcn_wave_barrier();
;         si[lane] = e0n; si[64 + lane] = e1n;
;         sc[lane] = g0n; sc[64 + lane] = g1n;
;         __builtin_amdgcn_wave_barrier();
;         f32x2 acc[16];
; #pragma unroll
;         for (int e = 0; e < 16; ++e) acc[e] = f32x2{0.f, 0.f};
;         const __amdgpu_buffer_rsrc_t vrs = __builtin_amdgcn_make_buffer_rsrc((void*)p.V8, 0, 0x2000000, 0x00020000);
;         const int voff = (int)x * (16384 * 128) + cc * 16;
;         uint4 qa[4], qb[4], qc[4], qd[4];
;     ...
;         EV_LOADN(qa, 0, 4); EV_LOADN(qb, 4, 4); EV_LOADN(qc, 8, 4); EV_LOADN(qd, 12, 4);
;         {
;           const int t1 = (tt + 1 < 16) ? t + 1 : t;
;           e0n = p.idx[(size_t)t1 * 128 + lane]; e1n = p.idx[(size_t)t1 * 128 + 64 + lane];
;           g0n = p.gate[(size_t)t1 * 128 + lane]; g1n = p.gate[(size_t)t1 * 128 + 64 + lane];
;         }
.LBB0_1391:
	s_or_b64 exec, exec, s[18:19]
	s_waitcnt lgkmcnt(0)
	s_barrier
	ds_read_b32 v0, v47
	s_waitcnt lgkmcnt(0)
	v_cmp_gt_i32_e32 vcc, 0, v0
	s_cbranch_vccnz .LBB0_1380
	v_lshl_add_u32 v50, v0, 6, v45
	v_ashrrev_i32_e32 v51, 31, v50
	v_lshlrev_b64 v[0:1], 9, v[50:51]
	v_lshl_or_b32 v0, v44, 2, v0
	v_lshl_add_u64 v[2:3], s[10:11], 0, v[0:1]
	v_lshl_add_u64 v[0:1], s[8:9], 0, v[0:1]
	global_load_dword v64, v[2:3], off
	global_load_dword v65, v[2:3], off offset:256
	global_load_dword v66, v[0:1], off
	global_load_dword v67, v[0:1], off offset:256
	ds_read_b32 v0, v47 offset:4
	s_mov_b64 s[18:19], 0
	s_waitcnt lgkmcnt(0)
	v_lshl_or_b32 v63, v0, 21, v55
	v_lshlrev_b32_e32 v46, 8, v0
	v_lshlrev_b64 v[0:1], 12, v[50:51]
	v_lshl_add_u64 v[0:1], v[46:47], 1, v[0:1]
	v_lshl_add_u64 v[52:53], v[48:49], 0, v[0:1]
	s_waitcnt vmcnt(0)
	ds_write2_b32 v54, v64, v65 offset0:16 offset1:80
	ds_write2_b32 v54, v66, v67 offset0:144 offset1:208
	ds_read2_b32 v[200:201], v56 offset0:16 offset1:24
	ds_read2_b32 v[202:203], v56 offset0:32 offset1:40
	ds_read2_b32 v[204:205], v56 offset0:48 offset1:56
	ds_read2_b32 v[206:207], v56 offset0:64 offset1:72
	ds_read2_b32 v[208:209], v56 offset0:80 offset1:88
	ds_read2_b32 v[210:211], v56 offset0:96 offset1:104
	ds_read2_b32 v[212:213], v56 offset0:112 offset1:120
	ds_read2_b32 v[214:215], v56 offset0:128 offset1:136
	s_cmpk_lg_u32 s18, 0xfff0
	s_cselect_b64 s[20:21], -1, 0
	v_cndmask_b32_e64 v64, 0, 1, s[20:21]
	v_mov_b32_e32 v65, s37
	v_lshl_add_u64 v[64:65], v[50:51], 0, v[64:65]
	v_lshlrev_b64 v[66:67], 9, v[64:65]
	v_mov_b32_e32 v50, v64
	v_mov_b32_e32 v51, v65
	v_lshl_or_b32 v66, v44, 2, v66
	v_lshl_add_u64 v[88:89], s[10:11], 0, v[66:67]
	s_waitcnt lgkmcnt(7)
	v_lshl_add_u32 v168, v200, 7, v63
	buffer_load_dwordx4 v[68:71], v168, s[12:15], 0 offen sc0
	v_lshl_add_u32 v168, v201, 7, v63
	buffer_load_dwordx4 v[72:75], v168, s[12:15], 0 offen sc0
	s_waitcnt lgkmcnt(6)
	v_lshl_add_u32 v168, v202, 7, v63
	buffer_load_dwordx4 v[76:79], v168, s[12:15], 0 offen sc0
	v_lshl_add_u32 v168, v203, 7, v63
	buffer_load_dwordx4 v[80:83], v168, s[12:15], 0 offen sc0
	s_waitcnt lgkmcnt(5)
	v_lshl_add_u32 v168, v204, 7, v63
	buffer_load_dwordx4 v[84:87], v168, s[12:15], 0 offen sc0
	v_lshl_add_u32 v168, v205, 7, v63
	buffer_load_dwordx4 v[40:43], v168, s[12:15], 0 offen sc0
	s_waitcnt lgkmcnt(4)
	v_lshl_add_u32 v168, v206, 7, v63
	buffer_load_dwordx4 v[36:39], v168, s[12:15], 0 offen sc0
	v_lshl_add_u32 v168, v207, 7, v63
	buffer_load_dwordx4 v[32:35], v168, s[12:15], 0 offen sc0
	s_waitcnt lgkmcnt(3)
	v_lshl_add_u32 v168, v208, 7, v63
	buffer_load_dwordx4 v[28:31], v168, s[12:15], 0 offen sc0
	v_lshl_add_u32 v168, v209, 7, v63
	buffer_load_dwordx4 v[24:27], v168, s[12:15], 0 offen sc0
	s_waitcnt lgkmcnt(2)
	v_lshl_add_u32 v168, v210, 7, v63
	buffer_load_dwordx4 v[20:23], v168, s[12:15], 0 offen sc0
	v_lshl_add_u32 v168, v211, 7, v63
	buffer_load_dwordx4 v[16:19], v168, s[12:15], 0 offen sc0
	s_waitcnt lgkmcnt(1)
	v_lshl_add_u32 v168, v212, 7, v63
	buffer_load_dwordx4 v[12:15], v168, s[12:15], 0 offen sc0
	v_lshl_add_u32 v168, v213, 7, v63
	buffer_load_dwordx4 v[8:11], v168, s[12:15], 0 offen sc0
	s_waitcnt lgkmcnt(0)
	v_lshl_add_u32 v168, v214, 7, v63
	buffer_load_dwordx4 v[4:7], v168, s[12:15], 0 offen sc0
	v_lshl_add_u32 v168, v215, 7, v63
	buffer_load_dwordx4 v[0:3], v168, s[12:15], 0 offen sc0
	s_nop 0
	global_load_dword v64, v[88:89], off
	global_load_dword v65, v[88:89], off offset:256
	v_lshl_add_u64 v[88:89], s[8:9], 0, v[66:67]
	global_load_dword v66, v[88:89], off
	global_load_dword v67, v[88:89], off offset:256
.LBB0_1393:
	ds_read2_b32 v[216:217], v56 offset0:144 offset1:152
	ds_read2_b32 v[218:219], v56 offset0:160 offset1:168
	ds_read2_b32 v[220:221], v56 offset0:176 offset1:184
	ds_read2_b32 v[222:223], v56 offset0:192 offset1:200
	ds_read2_b32 v[224:225], v56 offset0:208 offset1:216
	ds_read2_b32 v[226:227], v56 offset0:224 offset1:232
	ds_read2_b32 v[228:229], v56 offset0:240 offset1:248
	ds_read2_b32 v[230:231], v61 offset1:8
	s_waitcnt lgkmcnt(0)
	s_waitcnt vmcnt(19)
	v_cvt_scalef32_pk_f32_fp4 v[152:153], v68, 1.0
	v_cvt_scalef32_pk_f32_fp4 v[154:155], v68, 1.0 op_sel:[1,0,0]
	v_cvt_scalef32_pk_f32_fp4 v[156:157], v68, 1.0 op_sel:[0,1,0]
	v_cvt_scalef32_pk_f32_fp4 v[158:159], v68, 1.0 op_sel:[1,1,0]
	v_cvt_scalef32_pk_f32_fp4 v[160:161], v69, 1.0
	v_pk_mul_f32 v[120:121], v[216:217], v[152:153] op_sel_hi:[0,1]
	v_cvt_scalef32_pk_f32_fp4 v[162:163], v69, 1.0 op_sel:[1,0,0]
	v_pk_mul_f32 v[122:123], v[216:217], v[154:155] op_sel_hi:[0,1]
	v_cvt_scalef32_pk_f32_fp4 v[152:153], v69, 1.0 op_sel:[0,1,0]
	v_pk_mul_f32 v[124:125], v[216:217], v[156:157] op_sel_hi:[0,1]
	v_cvt_scalef32_pk_f32_fp4 v[154:155], v69, 1.0 op_sel:[1,1,0]
	v_pk_mul_f32 v[126:127], v[216:217], v[158:159] op_sel_hi:[0,1]
	v_cvt_scalef32_pk_f32_fp4 v[156:157], v70, 1.0
	v_pk_mul_f32 v[128:129], v[216:217], v[160:161] op_sel_hi:[0,1]
	v_cvt_scalef32_pk_f32_fp4 v[158:159], v70, 1.0 op_sel:[1,0,0]
	v_pk_mul_f32 v[130:131], v[216:217], v[162:163] op_sel_hi:[0,1]
	v_cvt_scalef32_pk_f32_fp4 v[160:161], v70, 1.0 op_sel:[0,1,0]
	v_pk_mul_f32 v[132:133], v[216:217], v[152:153] op_sel_hi:[0,1]
	v_cvt_scalef32_pk_f32_fp4 v[162:163], v70, 1.0 op_sel:[1,1,0]
	v_pk_mul_f32 v[134:135], v[216:217], v[154:155] op_sel_hi:[0,1]
	v_cvt_scalef32_pk_f32_fp4 v[152:153], v71, 1.0
	v_pk_mul_f32 v[136:137], v[216:217], v[156:157] op_sel_hi:[0,1]
	v_cvt_scalef32_pk_f32_fp4 v[154:155], v71, 1.0 op_sel:[1,0,0]
	v_pk_mul_f32 v[138:139], v[216:217], v[158:159] op_sel_hi:[0,1]
	v_cvt_scalef32_pk_f32_fp4 v[156:157], v71, 1.0 op_sel:[0,1,0]
	v_pk_mul_f32 v[140:141], v[216:217], v[160:161] op_sel_hi:[0,1]
	v_cvt_scalef32_pk_f32_fp4 v[158:159], v71, 1.0 op_sel:[1,1,0]
	v_pk_mul_f32 v[142:143], v[216:217], v[162:163] op_sel_hi:[0,1]
	v_pk_mul_f32 v[144:145], v[216:217], v[152:153] op_sel_hi:[0,1]
	v_pk_mul_f32 v[146:147], v[216:217], v[154:155] op_sel_hi:[0,1]
	v_pk_mul_f32 v[148:149], v[216:217], v[156:157] op_sel_hi:[0,1]
	v_pk_mul_f32 v[150:151], v[216:217], v[158:159] op_sel_hi:[0,1]
	s_waitcnt vmcnt(18)
	v_cvt_scalef32_pk_f32_fp4 v[152:153], v72, 1.0
	v_cvt_scalef32_pk_f32_fp4 v[154:155], v72, 1.0 op_sel:[1,0,0]
	v_cvt_scalef32_pk_f32_fp4 v[156:157], v72, 1.0 op_sel:[0,1,0]
	v_cvt_scalef32_pk_f32_fp4 v[158:159], v72, 1.0 op_sel:[1,1,0]
	v_cvt_scalef32_pk_f32_fp4 v[160:161], v73, 1.0
	v_pk_fma_f32 v[120:121], v[216:217], v[152:153], v[120:121] op_sel:[1,0,0] op_sel_hi:[1,1,1]
	v_cvt_scalef32_pk_f32_fp4 v[162:163], v73, 1.0 op_sel:[1,0,0]
	v_pk_fma_f32 v[122:123], v[216:217], v[154:155], v[122:123] op_sel:[1,0,0] op_sel_hi:[1,1,1]
	v_cvt_scalef32_pk_f32_fp4 v[152:153], v73, 1.0 op_sel:[0,1,0]
	v_pk_fma_f32 v[124:125], v[216:217], v[156:157], v[124:125] op_sel:[1,0,0] op_sel_hi:[1,1,1]
	v_cvt_scalef32_pk_f32_fp4 v[154:155], v73, 1.0 op_sel:[1,1,0]
	v_pk_fma_f32 v[126:127], v[216:217], v[158:159], v[126:127] op_sel:[1,0,0] op_sel_hi:[1,1,1]
	v_cvt_scalef32_pk_f32_fp4 v[156:157], v74, 1.0
	v_pk_fma_f32 v[128:129], v[216:217], v[160:161], v[128:129] op_sel:[1,0,0] op_sel_hi:[1,1,1]
	v_cvt_scalef32_pk_f32_fp4 v[158:159], v74, 1.0 op_sel:[1,0,0]
	v_pk_fma_f32 v[130:131], v[216:217], v[162:163], v[130:131] op_sel:[1,0,0] op_sel_hi:[1,1,1]
	v_cvt_scalef32_pk_f32_fp4 v[160:161], v74, 1.0 op_sel:[0,1,0]
	v_pk_fma_f32 v[132:133], v[216:217], v[152:153], v[132:133] op_sel:[1,0,0] op_sel_hi:[1,1,1]
	v_cvt_scalef32_pk_f32_fp4 v[162:163], v74, 1.0 op_sel:[1,1,0]
	v_pk_fma_f32 v[134:135], v[216:217], v[154:155], v[134:135] op_sel:[1,0,0] op_sel_hi:[1,1,1]
	v_cvt_scalef32_pk_f32_fp4 v[152:153], v75, 1.0
	v_pk_fma_f32 v[136:137], v[216:217], v[156:157], v[136:137] op_sel:[1,0,0] op_sel_hi:[1,1,1]
	v_cvt_scalef32_pk_f32_fp4 v[154:155], v75, 1.0 op_sel:[1,0,0]
	v_pk_fma_f32 v[138:139], v[216:217], v[158:159], v[138:139] op_sel:[1,0,0] op_sel_hi:[1,1,1]
	v_cvt_scalef32_pk_f32_fp4 v[156:157], v75, 1.0 op_sel:[0,1,0]
	v_pk_fma_f32 v[140:141], v[216:217], v[160:161], v[140:141] op_sel:[1,0,0] op_sel_hi:[1,1,1]
	v_cvt_scalef32_pk_f32_fp4 v[158:159], v75, 1.0 op_sel:[1,1,0]
	v_pk_fma_f32 v[142:143], v[216:217], v[162:163], v[142:143] op_sel:[1,0,0] op_sel_hi:[1,1,1]
	v_pk_fma_f32 v[144:145], v[216:217], v[152:153], v[144:145] op_sel:[1,0,0] op_sel_hi:[1,1,1]
	v_pk_fma_f32 v[146:147], v[216:217], v[154:155], v[146:147] op_sel:[1,0,0] op_sel_hi:[1,1,1]
	v_pk_fma_f32 v[148:149], v[216:217], v[156:157], v[148:149] op_sel:[1,0,0] op_sel_hi:[1,1,1]
	v_pk_fma_f32 v[150:151], v[216:217], v[158:159], v[150:151] op_sel:[1,0,0] op_sel_hi:[1,1,1]
	s_waitcnt vmcnt(17)
	v_cvt_scalef32_pk_f32_fp4 v[152:153], v76, 1.0
	v_cvt_scalef32_pk_f32_fp4 v[154:155], v76, 1.0 op_sel:[1,0,0]
	v_cvt_scalef32_pk_f32_fp4 v[156:157], v76, 1.0 op_sel:[0,1,0]
	v_cvt_scalef32_pk_f32_fp4 v[158:159], v76, 1.0 op_sel:[1,1,0]
	v_cvt_scalef32_pk_f32_fp4 v[160:161], v77, 1.0
	v_pk_fma_f32 v[120:121], v[218:219], v[152:153], v[120:121] op_sel_hi:[0,1,1]
	v_cvt_scalef32_pk_f32_fp4 v[162:163], v77, 1.0 op_sel:[1,0,0]
	v_pk_fma_f32 v[122:123], v[218:219], v[154:155], v[122:123] op_sel_hi:[0,1,1]
	v_cvt_scalef32_pk_f32_fp4 v[152:153], v77, 1.0 op_sel:[0,1,0]
	v_pk_fma_f32 v[124:125], v[218:219], v[156:157], v[124:125] op_sel_hi:[0,1,1]
	v_cvt_scalef32_pk_f32_fp4 v[154:155], v77, 1.0 op_sel:[1,1,0]
	v_pk_fma_f32 v[126:127], v[218:219], v[158:159], v[126:127] op_sel_hi:[0,1,1]
	v_cvt_scalef32_pk_f32_fp4 v[156:157], v78, 1.0
	v_pk_fma_f32 v[128:129], v[218:219], v[160:161], v[128:129] op_sel_hi:[0,1,1]
	v_cvt_scalef32_pk_f32_fp4 v[158:159], v78, 1.0 op_sel:[1,0,0]
	v_pk_fma_f32 v[130:131], v[218:219], v[162:163], v[130:131] op_sel_hi:[0,1,1]
	v_cvt_scalef32_pk_f32_fp4 v[160:161], v78, 1.0 op_sel:[0,1,0]
	v_pk_fma_f32 v[132:133], v[218:219], v[152:153], v[132:133] op_sel_hi:[0,1,1]
	v_cvt_scalef32_pk_f32_fp4 v[162:163], v78, 1.0 op_sel:[1,1,0]
	v_pk_fma_f32 v[134:135], v[218:219], v[154:155], v[134:135] op_sel_hi:[0,1,1]
	v_cvt_scalef32_pk_f32_fp4 v[152:153], v79, 1.0
	v_pk_fma_f32 v[136:137], v[218:219], v[156:157], v[136:137] op_sel_hi:[0,1,1]
	v_cvt_scalef32_pk_f32_fp4 v[154:155], v79, 1.0 op_sel:[1,0,0]
	v_pk_fma_f32 v[138:139], v[218:219], v[158:159], v[138:139] op_sel_hi:[0,1,1]
	v_cvt_scalef32_pk_f32_fp4 v[156:157], v79, 1.0 op_sel:[0,1,0]
	v_pk_fma_f32 v[140:141], v[218:219], v[160:161], v[140:141] op_sel_hi:[0,1,1]
	v_cvt_scalef32_pk_f32_fp4 v[158:159], v79, 1.0 op_sel:[1,1,0]
	v_pk_fma_f32 v[142:143], v[218:219], v[162:163], v[142:143] op_sel_hi:[0,1,1]
	v_pk_fma_f32 v[144:145], v[218:219], v[152:153], v[144:145] op_sel_hi:[0,1,1]
	v_pk_fma_f32 v[146:147], v[218:219], v[154:155], v[146:147] op_sel_hi:[0,1,1]
	v_pk_fma_f32 v[148:149], v[218:219], v[156:157], v[148:149] op_sel_hi:[0,1,1]
	v_pk_fma_f32 v[150:151], v[218:219], v[158:159], v[150:151] op_sel_hi:[0,1,1]
	s_waitcnt vmcnt(16)
; #define EV_LOADN(q_, g0_, n_) _Pragma("unroll") for (int k = 0; k < (n_); ++k) q_[k] = __builtin_bit_cast(uint4, __builtin_amdgcn_raw_buffer_load_b128(vrs, voff + si[((g0_) + k) * 8 + sub] * 128, 0, GATHER_AUX))
; __device__ void phase_exp_v(KParams& p, char* smem) {
;     ...
;         EV_LOADN(qa, 0, 4); EV_LOADN(qb, 4, 4); EV_LOADN(qc, 8, 4); EV_LOADN(qd, 12, 4);
;         {
;           const int t1 = (tt + 1 < 16) ? t + 1 : t;
;           e0n = p.idx[(size_t)t1 * 128 + lane]; e1n = p.idx[(size_t)t1 * 128 + 64 + lane];
;           g0n = p.gate[(size_t)t1 * 128 + lane]; g1n = p.gate[(size_t)t1 * 128 + 64 + lane];
;         }
	v_cvt_scalef32_pk_f32_fp4 v[152:153], v80, 1.0
	v_cvt_scalef32_pk_f32_fp4 v[154:155], v80, 1.0 op_sel:[1,0,0]
	v_cvt_scalef32_pk_f32_fp4 v[156:157], v80, 1.0 op_sel:[0,1,0]
	v_cvt_scalef32_pk_f32_fp4 v[158:159], v80, 1.0 op_sel:[1,1,0]
	v_cvt_scalef32_pk_f32_fp4 v[160:161], v81, 1.0
	v_pk_fma_f32 v[120:121], v[218:219], v[152:153], v[120:121] op_sel:[1,0,0] op_sel_hi:[1,1,1]
	v_cvt_scalef32_pk_f32_fp4 v[162:163], v81, 1.0 op_sel:[1,0,0]
	v_pk_fma_f32 v[122:123], v[218:219], v[154:155], v[122:123] op_sel:[1,0,0] op_sel_hi:[1,1,1]
	v_cvt_scalef32_pk_f32_fp4 v[152:153], v81, 1.0 op_sel:[0,1,0]
	v_pk_fma_f32 v[124:125], v[218:219], v[156:157], v[124:125] op_sel:[1,0,0] op_sel_hi:[1,1,1]
	v_cvt_scalef32_pk_f32_fp4 v[154:155], v81, 1.0 op_sel:[1,1,0]
	v_pk_fma_f32 v[126:127], v[218:219], v[158:159], v[126:127] op_sel:[1,0,0] op_sel_hi:[1,1,1]
	v_cvt_scalef32_pk_f32_fp4 v[156:157], v82, 1.0
	v_pk_fma_f32 v[128:129], v[218:219], v[160:161], v[128:129] op_sel:[1,0,0] op_sel_hi:[1,1,1]
	v_cvt_scalef32_pk_f32_fp4 v[158:159], v82, 1.0 op_sel:[1,0,0]
	v_pk_fma_f32 v[130:131], v[218:219], v[162:163], v[130:131] op_sel:[1,0,0] op_sel_hi:[1,1,1]
	v_cvt_scalef32_pk_f32_fp4 v[160:161], v82, 1.0 op_sel:[0,1,0]
	v_pk_fma_f32 v[132:133], v[218:219], v[152:153], v[132:133] op_sel:[1,0,0] op_sel_hi:[1,1,1]
	v_cvt_scalef32_pk_f32_fp4 v[162:163], v82, 1.0 op_sel:[1,1,0]
	v_pk_fma_f32 v[134:135], v[218:219], v[154:155], v[134:135] op_sel:[1,0,0] op_sel_hi:[1,1,1]
	v_cvt_scalef32_pk_f32_fp4 v[152:153], v83, 1.0
	v_pk_fma_f32 v[136:137], v[218:219], v[156:157], v[136:137] op_sel:[1,0,0] op_sel_hi:[1,1,1]
	v_cvt_scalef32_pk_f32_fp4 v[154:155], v83, 1.0 op_sel:[1,0,0]
	v_pk_fma_f32 v[138:139], v[218:219], v[158:159], v[138:139] op_sel:[1,0,0] op_sel_hi:[1,1,1]
	v_cvt_scalef32_pk_f32_fp4 v[156:157], v83, 1.0 op_sel:[0,1,0]
	v_pk_fma_f32 v[140:141], v[218:219], v[160:161], v[140:141] op_sel:[1,0,0] op_sel_hi:[1,1,1]
	v_cvt_scalef32_pk_f32_fp4 v[158:159], v83, 1.0 op_sel:[1,1,0]
	v_pk_fma_f32 v[142:143], v[218:219], v[162:163], v[142:143] op_sel:[1,0,0] op_sel_hi:[1,1,1]
	v_pk_fma_f32 v[144:145], v[218:219], v[152:153], v[144:145] op_sel:[1,0,0] op_sel_hi:[1,1,1]
	v_pk_fma_f32 v[146:147], v[218:219], v[154:155], v[146:147] op_sel:[1,0,0] op_sel_hi:[1,1,1]
	v_pk_fma_f32 v[148:149], v[218:219], v[156:157], v[148:149] op_sel:[1,0,0] op_sel_hi:[1,1,1]
	v_pk_fma_f32 v[150:151], v[218:219], v[158:159], v[150:151] op_sel:[1,0,0] op_sel_hi:[1,1,1]
	s_waitcnt vmcnt(0)
	ds_write2_b32 v54, v64, v65 offset0:16 offset1:80
	ds_write2_b32 v54, v66, v67 offset0:144 offset1:208
	ds_read2_b32 v[200:201], v56 offset0:16 offset1:24
	ds_read2_b32 v[202:203], v56 offset0:32 offset1:40
	ds_read2_b32 v[204:205], v56 offset0:48 offset1:56
	ds_read2_b32 v[206:207], v56 offset0:64 offset1:72
	ds_read2_b32 v[208:209], v56 offset0:80 offset1:88
	ds_read2_b32 v[210:211], v56 offset0:96 offset1:104
	ds_read2_b32 v[212:213], v56 offset0:112 offset1:120
	ds_read2_b32 v[214:215], v56 offset0:128 offset1:136
	s_cmpk_lg_u32 s18, 0xe000
	s_cselect_b64 s[20:21], -1, 0
	v_cndmask_b32_e64 v64, 0, 1, s[20:21]
	v_mov_b32_e32 v65, s37
	v_lshl_add_u64 v[64:65], v[50:51], 0, v[64:65]
	v_lshlrev_b64 v[66:67], 9, v[64:65]
	v_mov_b32_e32 v50, v64
	v_mov_b32_e32 v51, v65
	v_lshl_or_b32 v66, v44, 2, v66
	v_lshl_add_u64 v[88:89], s[10:11], 0, v[66:67]
	s_waitcnt lgkmcnt(7)
	v_lshl_add_u32 v168, v200, 7, v63
	buffer_load_dwordx4 v[90:93], v168, s[12:15], 0 offen sc0
	v_lshl_add_u32 v168, v201, 7, v63
	buffer_load_dwordx4 v[94:97], v168, s[12:15], 0 offen sc0
	s_waitcnt lgkmcnt(6)
	v_lshl_add_u32 v168, v202, 7, v63
	buffer_load_dwordx4 v[98:101], v168, s[12:15], 0 offen sc0
	v_lshl_add_u32 v168, v203, 7, v63
	buffer_load_dwordx4 v[102:105], v168, s[12:15], 0 offen sc0
	s_waitcnt lgkmcnt(5)
	v_lshl_add_u32 v168, v204, 7, v63
	buffer_load_dwordx4 v[106:109], v168, s[12:15], 0 offen sc0
	v_lshl_add_u32 v168, v205, 7, v63
	buffer_load_dwordx4 v[110:113], v168, s[12:15], 0 offen sc0
	s_waitcnt lgkmcnt(4)
	v_lshl_add_u32 v168, v206, 7, v63
	buffer_load_dwordx4 v[114:117], v168, s[12:15], 0 offen sc0
	v_lshl_add_u32 v168, v207, 7, v63
	buffer_load_dwordx4 v[232:235], v168, s[12:15], 0 offen sc0
	s_waitcnt lgkmcnt(3)
	v_lshl_add_u32 v168, v208, 7, v63
	buffer_load_dwordx4 v[236:239], v168, s[12:15], 0 offen sc0
	v_lshl_add_u32 v168, v209, 7, v63
	buffer_load_dwordx4 v[240:243], v168, s[12:15], 0 offen sc0
	s_waitcnt lgkmcnt(2)
	v_lshl_add_u32 v168, v210, 7, v63
	buffer_load_dwordx4 v[244:247], v168, s[12:15], 0 offen sc0
	v_lshl_add_u32 v168, v211, 7, v63
	buffer_load_dwordx4 v[248:251], v168, s[12:15], 0 offen sc0
	s_waitcnt lgkmcnt(1)
	v_lshl_add_u32 v168, v212, 7, v63
	buffer_load_dwordx4 v[164:167], v168, s[12:15], 0 offen sc0
	v_lshl_add_u32 v168, v213, 7, v63
	buffer_load_dwordx4 v[172:175], v168, s[12:15], 0 offen sc0
	s_waitcnt lgkmcnt(0)
; #define EV_LOADN(q_, g0_, n_) _Pragma("unroll") for (int k = 0; k < (n_); ++k) q_[k] = __builtin_bit_cast(uint4, __builtin_amdgcn_raw_buffer_load_b128(vrs, voff + si[((g0_) + k) * 8 + sub] * 128, 0, GATHER_AUX))
; __device__ void phase_exp_v(KParams& p, char* smem) {
;     ...
;         EV_LOADN(qa, 0, 4); EV_LOADN(qb, 4, 4); EV_LOADN(qc, 8, 4); EV_LOADN(qd, 12, 4);
;         {
;           const int t1 = (tt + 1 < 16) ? t + 1 : t;
;           e0n = p.idx[(size_t)t1 * 128 + lane]; e1n = p.idx[(size_t)t1 * 128 + 64 + lane];
;           g0n = p.gate[(size_t)t1 * 128 + lane]; g1n = p.gate[(size_t)t1 * 128 + 64 + lane];
;         }
	v_lshl_add_u32 v168, v214, 7, v63
	buffer_load_dwordx4 v[192:195], v168, s[12:15], 0 offen sc0
	v_lshl_add_u32 v168, v215, 7, v63
	buffer_load_dwordx4 v[196:199], v168, s[12:15], 0 offen sc0
	s_nop 0
	global_load_dword v64, v[88:89], off
	global_load_dword v65, v[88:89], off offset:256
	v_lshl_add_u64 v[88:89], s[8:9], 0, v[66:67]
	global_load_dword v66, v[88:89], off
	global_load_dword v67, v[88:89], off offset:256
	v_cvt_scalef32_pk_f32_fp4 v[152:153], v84, 1.0
	v_cvt_scalef32_pk_f32_fp4 v[154:155], v84, 1.0 op_sel:[1,0,0]
	v_cvt_scalef32_pk_f32_fp4 v[156:157], v84, 1.0 op_sel:[0,1,0]
	v_cvt_scalef32_pk_f32_fp4 v[158:159], v84, 1.0 op_sel:[1,1,0]
	v_cvt_scalef32_pk_f32_fp4 v[160:161], v85, 1.0
	v_pk_fma_f32 v[120:121], v[220:221], v[152:153], v[120:121] op_sel_hi:[0,1,1]
	v_cvt_scalef32_pk_f32_fp4 v[162:163], v85, 1.0 op_sel:[1,0,0]
	v_pk_fma_f32 v[122:123], v[220:221], v[154:155], v[122:123] op_sel_hi:[0,1,1]
	v_cvt_scalef32_pk_f32_fp4 v[152:153], v85, 1.0 op_sel:[0,1,0]
	v_pk_fma_f32 v[124:125], v[220:221], v[156:157], v[124:125] op_sel_hi:[0,1,1]
	v_cvt_scalef32_pk_f32_fp4 v[154:155], v85, 1.0 op_sel:[1,1,0]
	v_pk_fma_f32 v[126:127], v[220:221], v[158:159], v[126:127] op_sel_hi:[0,1,1]
	v_cvt_scalef32_pk_f32_fp4 v[156:157], v86, 1.0
	v_pk_fma_f32 v[128:129], v[220:221], v[160:161], v[128:129] op_sel_hi:[0,1,1]
	v_cvt_scalef32_pk_f32_fp4 v[158:159], v86, 1.0 op_sel:[1,0,0]
	v_pk_fma_f32 v[130:131], v[220:221], v[162:163], v[130:131] op_sel_hi:[0,1,1]
	v_cvt_scalef32_pk_f32_fp4 v[160:161], v86, 1.0 op_sel:[0,1,0]
	v_pk_fma_f32 v[132:133], v[220:221], v[152:153], v[132:133] op_sel_hi:[0,1,1]
	v_cvt_scalef32_pk_f32_fp4 v[162:163], v86, 1.0 op_sel:[1,1,0]
	v_pk_fma_f32 v[134:135], v[220:221], v[154:155], v[134:135] op_sel_hi:[0,1,1]
	v_cvt_scalef32_pk_f32_fp4 v[152:153], v87, 1.0
	v_pk_fma_f32 v[136:137], v[220:221], v[156:157], v[136:137] op_sel_hi:[0,1,1]
	v_cvt_scalef32_pk_f32_fp4 v[154:155], v87, 1.0 op_sel:[1,0,0]
	v_pk_fma_f32 v[138:139], v[220:221], v[158:159], v[138:139] op_sel_hi:[0,1,1]
	v_cvt_scalef32_pk_f32_fp4 v[156:157], v87, 1.0 op_sel:[0,1,0]
	v_pk_fma_f32 v[140:141], v[220:221], v[160:161], v[140:141] op_sel_hi:[0,1,1]
	v_cvt_scalef32_pk_f32_fp4 v[158:159], v87, 1.0 op_sel:[1,1,0]
	v_pk_fma_f32 v[142:143], v[220:221], v[162:163], v[142:143] op_sel_hi:[0,1,1]
	v_pk_fma_f32 v[144:145], v[220:221], v[152:153], v[144:145] op_sel_hi:[0,1,1]
	v_pk_fma_f32 v[146:147], v[220:221], v[154:155], v[146:147] op_sel_hi:[0,1,1]
	v_pk_fma_f32 v[148:149], v[220:221], v[156:157], v[148:149] op_sel_hi:[0,1,1]
	v_pk_fma_f32 v[150:151], v[220:221], v[158:159], v[150:151] op_sel_hi:[0,1,1]
	v_cvt_scalef32_pk_f32_fp4 v[152:153], v40, 1.0
	v_cvt_scalef32_pk_f32_fp4 v[154:155], v40, 1.0 op_sel:[1,0,0]
	v_cvt_scalef32_pk_f32_fp4 v[156:157], v40, 1.0 op_sel:[0,1,0]
	v_cvt_scalef32_pk_f32_fp4 v[158:159], v40, 1.0 op_sel:[1,1,0]
	v_cvt_scalef32_pk_f32_fp4 v[160:161], v41, 1.0
	v_pk_fma_f32 v[120:121], v[220:221], v[152:153], v[120:121] op_sel:[1,0,0] op_sel_hi:[1,1,1]
	v_cvt_scalef32_pk_f32_fp4 v[162:163], v41, 1.0 op_sel:[1,0,0]
	v_pk_fma_f32 v[122:123], v[220:221], v[154:155], v[122:123] op_sel:[1,0,0] op_sel_hi:[1,1,1]
	v_cvt_scalef32_pk_f32_fp4 v[152:153], v41, 1.0 op_sel:[0,1,0]
	v_pk_fma_f32 v[124:125], v[220:221], v[156:157], v[124:125] op_sel:[1,0,0] op_sel_hi:[1,1,1]
	v_cvt_scalef32_pk_f32_fp4 v[154:155], v41, 1.0 op_sel:[1,1,0]
	v_pk_fma_f32 v[126:127], v[220:221], v[158:159], v[126:127] op_sel:[1,0,0] op_sel_hi:[1,1,1]
	v_cvt_scalef32_pk_f32_fp4 v[156:157], v42, 1.0
	v_pk_fma_f32 v[128:129], v[220:221], v[160:161], v[128:129] op_sel:[1,0,0] op_sel_hi:[1,1,1]
	v_cvt_scalef32_pk_f32_fp4 v[158:159], v42, 1.0 op_sel:[1,0,0]
	v_pk_fma_f32 v[130:131], v[220:221], v[162:163], v[130:131] op_sel:[1,0,0] op_sel_hi:[1,1,1]
	v_cvt_scalef32_pk_f32_fp4 v[160:161], v42, 1.0 op_sel:[0,1,0]
	v_pk_fma_f32 v[132:133], v[220:221], v[152:153], v[132:133] op_sel:[1,0,0] op_sel_hi:[1,1,1]
	v_cvt_scalef32_pk_f32_fp4 v[162:163], v42, 1.0 op_sel:[1,1,0]
	v_pk_fma_f32 v[134:135], v[220:221], v[154:155], v[134:135] op_sel:[1,0,0] op_sel_hi:[1,1,1]
	v_cvt_scalef32_pk_f32_fp4 v[152:153], v43, 1.0
	v_pk_fma_f32 v[136:137], v[220:221], v[156:157], v[136:137] op_sel:[1,0,0] op_sel_hi:[1,1,1]
	v_cvt_scalef32_pk_f32_fp4 v[154:155], v43, 1.0 op_sel:[1,0,0]
	v_pk_fma_f32 v[138:139], v[220:221], v[158:159], v[138:139] op_sel:[1,0,0] op_sel_hi:[1,1,1]
	v_cvt_scalef32_pk_f32_fp4 v[156:157], v43, 1.0 op_sel:[0,1,0]
	v_pk_fma_f32 v[140:141], v[220:221], v[160:161], v[140:141] op_sel:[1,0,0] op_sel_hi:[1,1,1]
	v_cvt_scalef32_pk_f32_fp4 v[158:159], v43, 1.0 op_sel:[1,1,0]
	v_pk_fma_f32 v[142:143], v[220:221], v[162:163], v[142:143] op_sel:[1,0,0] op_sel_hi:[1,1,1]
	v_pk_fma_f32 v[144:145], v[220:221], v[152:153], v[144:145] op_sel:[1,0,0] op_sel_hi:[1,1,1]
	v_pk_fma_f32 v[146:147], v[220:221], v[154:155], v[146:147] op_sel:[1,0,0] op_sel_hi:[1,1,1]
	v_pk_fma_f32 v[148:149], v[220:221], v[156:157], v[148:149] op_sel:[1,0,0] op_sel_hi:[1,1,1]
	v_pk_fma_f32 v[150:151], v[220:221], v[158:159], v[150:151] op_sel:[1,0,0] op_sel_hi:[1,1,1]
	v_cvt_scalef32_pk_f32_fp4 v[152:153], v36, 1.0
	v_cvt_scalef32_pk_f32_fp4 v[154:155], v36, 1.0 op_sel:[1,0,0]
	v_cvt_scalef32_pk_f32_fp4 v[156:157], v36, 1.0 op_sel:[0,1,0]
	v_cvt_scalef32_pk_f32_fp4 v[158:159], v36, 1.0 op_sel:[1,1,0]
	v_cvt_scalef32_pk_f32_fp4 v[160:161], v37, 1.0
	v_pk_fma_f32 v[120:121], v[222:223], v[152:153], v[120:121] op_sel_hi:[0,1,1]
	v_cvt_scalef32_pk_f32_fp4 v[162:163], v37, 1.0 op_sel:[1,0,0]
	v_pk_fma_f32 v[122:123], v[222:223], v[154:155], v[122:123] op_sel_hi:[0,1,1]
	v_cvt_scalef32_pk_f32_fp4 v[152:153], v37, 1.0 op_sel:[0,1,0]
	v_pk_fma_f32 v[124:125], v[222:223], v[156:157], v[124:125] op_sel_hi:[0,1,1]
	v_cvt_scalef32_pk_f32_fp4 v[154:155], v37, 1.0 op_sel:[1,1,0]
	v_pk_fma_f32 v[126:127], v[222:223], v[158:159], v[126:127] op_sel_hi:[0,1,1]
	v_cvt_scalef32_pk_f32_fp4 v[156:157], v38, 1.0
	v_pk_fma_f32 v[128:129], v[222:223], v[160:161], v[128:129] op_sel_hi:[0,1,1]
	v_cvt_scalef32_pk_f32_fp4 v[158:159], v38, 1.0 op_sel:[1,0,0]
	v_pk_fma_f32 v[130:131], v[222:223], v[162:163], v[130:131] op_sel_hi:[0,1,1]
	v_cvt_scalef32_pk_f32_fp4 v[160:161], v38, 1.0 op_sel:[0,1,0]
	v_pk_fma_f32 v[132:133], v[222:223], v[152:153], v[132:133] op_sel_hi:[0,1,1]
	v_cvt_scalef32_pk_f32_fp4 v[162:163], v38, 1.0 op_sel:[1,1,0]
	v_pk_fma_f32 v[134:135], v[222:223], v[154:155], v[134:135] op_sel_hi:[0,1,1]
	v_cvt_scalef32_pk_f32_fp4 v[152:153], v39, 1.0
	v_pk_fma_f32 v[136:137], v[222:223], v[156:157], v[136:137] op_sel_hi:[0,1,1]
	v_cvt_scalef32_pk_f32_fp4 v[154:155], v39, 1.0 op_sel:[1,0,0]
	v_pk_fma_f32 v[138:139], v[222:223], v[158:159], v[138:139] op_sel_hi:[0,1,1]
	v_cvt_scalef32_pk_f32_fp4 v[156:157], v39, 1.0 op_sel:[0,1,0]
	v_pk_fma_f32 v[140:141], v[222:223], v[160:161], v[140:141] op_sel_hi:[0,1,1]
	v_cvt_scalef32_pk_f32_fp4 v[158:159], v39, 1.0 op_sel:[1,1,0]
	v_pk_fma_f32 v[142:143], v[222:223], v[162:163], v[142:143] op_sel_hi:[0,1,1]
	v_pk_fma_f32 v[144:145], v[222:223], v[152:153], v[144:145] op_sel_hi:[0,1,1]
	v_pk_fma_f32 v[146:147], v[222:223], v[154:155], v[146:147] op_sel_hi:[0,1,1]
	v_pk_fma_f32 v[148:149], v[222:223], v[156:157], v[148:149] op_sel_hi:[0,1,1]
	v_pk_fma_f32 v[150:151], v[222:223], v[158:159], v[150:151] op_sel_hi:[0,1,1]
	v_cvt_scalef32_pk_f32_fp4 v[152:153], v32, 1.0
	v_cvt_scalef32_pk_f32_fp4 v[154:155], v32, 1.0 op_sel:[1,0,0]
	v_cvt_scalef32_pk_f32_fp4 v[156:157], v32, 1.0 op_sel:[0,1,0]
	v_cvt_scalef32_pk_f32_fp4 v[158:159], v32, 1.0 op_sel:[1,1,0]
	v_cvt_scalef32_pk_f32_fp4 v[160:161], v33, 1.0
	v_pk_fma_f32 v[120:121], v[222:223], v[152:153], v[120:121] op_sel:[1,0,0] op_sel_hi:[1,1,1]
	v_cvt_scalef32_pk_f32_fp4 v[162:163], v33, 1.0 op_sel:[1,0,0]
	v_pk_fma_f32 v[122:123], v[222:223], v[154:155], v[122:123] op_sel:[1,0,0] op_sel_hi:[1,1,1]
	v_cvt_scalef32_pk_f32_fp4 v[152:153], v33, 1.0 op_sel:[0,1,0]
	v_pk_fma_f32 v[124:125], v[222:223], v[156:157], v[124:125] op_sel:[1,0,0] op_sel_hi:[1,1,1]
	v_cvt_scalef32_pk_f32_fp4 v[154:155], v33, 1.0 op_sel:[1,1,0]
	v_pk_fma_f32 v[126:127], v[222:223], v[158:159], v[126:127] op_sel:[1,0,0] op_sel_hi:[1,1,1]
	v_cvt_scalef32_pk_f32_fp4 v[156:157], v34, 1.0
	v_pk_fma_f32 v[128:129], v[222:223], v[160:161], v[128:129] op_sel:[1,0,0] op_sel_hi:[1,1,1]
	v_cvt_scalef32_pk_f32_fp4 v[158:159], v34, 1.0 op_sel:[1,0,0]
	v_pk_fma_f32 v[130:131], v[222:223], v[162:163], v[130:131] op_sel:[1,0,0] op_sel_hi:[1,1,1]
	v_cvt_scalef32_pk_f32_fp4 v[160:161], v34, 1.0 op_sel:[0,1,0]
	v_pk_fma_f32 v[132:133], v[222:223], v[152:153], v[132:133] op_sel:[1,0,0] op_sel_hi:[1,1,1]
	v_cvt_scalef32_pk_f32_fp4 v[162:163], v34, 1.0 op_sel:[1,1,0]
	v_pk_fma_f32 v[134:135], v[222:223], v[154:155], v[134:135] op_sel:[1,0,0] op_sel_hi:[1,1,1]
	v_cvt_scalef32_pk_f32_fp4 v[152:153], v35, 1.0
	v_pk_fma_f32 v[136:137], v[222:223], v[156:157], v[136:137] op_sel:[1,0,0] op_sel_hi:[1,1,1]
	v_cvt_scalef32_pk_f32_fp4 v[154:155], v35, 1.0 op_sel:[1,0,0]
	v_pk_fma_f32 v[138:139], v[222:223], v[158:159], v[138:139] op_sel:[1,0,0] op_sel_hi:[1,1,1]
	v_cvt_scalef32_pk_f32_fp4 v[156:157], v35, 1.0 op_sel:[0,1,0]
	v_pk_fma_f32 v[140:141], v[222:223], v[160:161], v[140:141] op_sel:[1,0,0] op_sel_hi:[1,1,1]
	v_cvt_scalef32_pk_f32_fp4 v[158:159], v35, 1.0 op_sel:[1,1,0]
	v_pk_fma_f32 v[142:143], v[222:223], v[162:163], v[142:143] op_sel:[1,0,0] op_sel_hi:[1,1,1]
	v_pk_fma_f32 v[144:145], v[222:223], v[152:153], v[144:145] op_sel:[1,0,0] op_sel_hi:[1,1,1]
	v_pk_fma_f32 v[146:147], v[222:223], v[154:155], v[146:147] op_sel:[1,0,0] op_sel_hi:[1,1,1]
	v_pk_fma_f32 v[148:149], v[222:223], v[156:157], v[148:149] op_sel:[1,0,0] op_sel_hi:[1,1,1]
	v_pk_fma_f32 v[150:151], v[222:223], v[158:159], v[150:151] op_sel:[1,0,0] op_sel_hi:[1,1,1]
	v_cvt_scalef32_pk_f32_fp4 v[152:153], v28, 1.0
	v_cvt_scalef32_pk_f32_fp4 v[154:155], v28, 1.0 op_sel:[1,0,0]
	v_cvt_scalef32_pk_f32_fp4 v[156:157], v28, 1.0 op_sel:[0,1,0]
	v_cvt_scalef32_pk_f32_fp4 v[158:159], v28, 1.0 op_sel:[1,1,0]
	v_cvt_scalef32_pk_f32_fp4 v[160:161], v29, 1.0
	v_pk_fma_f32 v[120:121], v[224:225], v[152:153], v[120:121] op_sel_hi:[0,1,1]
	v_cvt_scalef32_pk_f32_fp4 v[162:163], v29, 1.0 op_sel:[1,0,0]
	v_pk_fma_f32 v[122:123], v[224:225], v[154:155], v[122:123] op_sel_hi:[0,1,1]
	v_cvt_scalef32_pk_f32_fp4 v[152:153], v29, 1.0 op_sel:[0,1,0]
	v_pk_fma_f32 v[124:125], v[224:225], v[156:157], v[124:125] op_sel_hi:[0,1,1]
	v_cvt_scalef32_pk_f32_fp4 v[154:155], v29, 1.0 op_sel:[1,1,0]
	v_pk_fma_f32 v[126:127], v[224:225], v[158:159], v[126:127] op_sel_hi:[0,1,1]
	v_cvt_scalef32_pk_f32_fp4 v[156:157], v30, 1.0
	v_pk_fma_f32 v[128:129], v[224:225], v[160:161], v[128:129] op_sel_hi:[0,1,1]
	v_cvt_scalef32_pk_f32_fp4 v[158:159], v30, 1.0 op_sel:[1,0,0]
	v_pk_fma_f32 v[130:131], v[224:225], v[162:163], v[130:131] op_sel_hi:[0,1,1]
	v_cvt_scalef32_pk_f32_fp4 v[160:161], v30, 1.0 op_sel:[0,1,0]
	v_pk_fma_f32 v[132:133], v[224:225], v[152:153], v[132:133] op_sel_hi:[0,1,1]
	v_cvt_scalef32_pk_f32_fp4 v[162:163], v30, 1.0 op_sel:[1,1,0]
	v_pk_fma_f32 v[134:135], v[224:225], v[154:155], v[134:135] op_sel_hi:[0,1,1]
	v_cvt_scalef32_pk_f32_fp4 v[152:153], v31, 1.0
	v_pk_fma_f32 v[136:137], v[224:225], v[156:157], v[136:137] op_sel_hi:[0,1,1]
	v_cvt_scalef32_pk_f32_fp4 v[154:155], v31, 1.0 op_sel:[1,0,0]
	v_pk_fma_f32 v[138:139], v[224:225], v[158:159], v[138:139] op_sel_hi:[0,1,1]
	v_cvt_scalef32_pk_f32_fp4 v[156:157], v31, 1.0 op_sel:[0,1,0]
	v_pk_fma_f32 v[140:141], v[224:225], v[160:161], v[140:141] op_sel_hi:[0,1,1]
	v_cvt_scalef32_pk_f32_fp4 v[158:159], v31, 1.0 op_sel:[1,1,0]
	v_pk_fma_f32 v[142:143], v[224:225], v[162:163], v[142:143] op_sel_hi:[0,1,1]
	v_pk_fma_f32 v[144:145], v[224:225], v[152:153], v[144:145] op_sel_hi:[0,1,1]
	v_pk_fma_f32 v[146:147], v[224:225], v[154:155], v[146:147] op_sel_hi:[0,1,1]
	v_pk_fma_f32 v[148:149], v[224:225], v[156:157], v[148:149] op_sel_hi:[0,1,1]
	v_pk_fma_f32 v[150:151], v[224:225], v[158:159], v[150:151] op_sel_hi:[0,1,1]
	v_cvt_scalef32_pk_f32_fp4 v[152:153], v24, 1.0
	v_cvt_scalef32_pk_f32_fp4 v[154:155], v24, 1.0 op_sel:[1,0,0]
	v_cvt_scalef32_pk_f32_fp4 v[156:157], v24, 1.0 op_sel:[0,1,0]
	v_cvt_scalef32_pk_f32_fp4 v[158:159], v24, 1.0 op_sel:[1,1,0]
	v_cvt_scalef32_pk_f32_fp4 v[160:161], v25, 1.0
	v_pk_fma_f32 v[120:121], v[224:225], v[152:153], v[120:121] op_sel:[1,0,0] op_sel_hi:[1,1,1]
	v_cvt_scalef32_pk_f32_fp4 v[162:163], v25, 1.0 op_sel:[1,0,0]
	v_pk_fma_f32 v[122:123], v[224:225], v[154:155], v[122:123] op_sel:[1,0,0] op_sel_hi:[1,1,1]
	v_cvt_scalef32_pk_f32_fp4 v[152:153], v25, 1.0 op_sel:[0,1,0]
	v_pk_fma_f32 v[124:125], v[224:225], v[156:157], v[124:125] op_sel:[1,0,0] op_sel_hi:[1,1,1]
	v_cvt_scalef32_pk_f32_fp4 v[154:155], v25, 1.0 op_sel:[1,1,0]
	v_pk_fma_f32 v[126:127], v[224:225], v[158:159], v[126:127] op_sel:[1,0,0] op_sel_hi:[1,1,1]
	v_cvt_scalef32_pk_f32_fp4 v[156:157], v26, 1.0
	v_pk_fma_f32 v[128:129], v[224:225], v[160:161], v[128:129] op_sel:[1,0,0] op_sel_hi:[1,1,1]
	v_cvt_scalef32_pk_f32_fp4 v[158:159], v26, 1.0 op_sel:[1,0,0]
	v_pk_fma_f32 v[130:131], v[224:225], v[162:163], v[130:131] op_sel:[1,0,0] op_sel_hi:[1,1,1]
	v_cvt_scalef32_pk_f32_fp4 v[160:161], v26, 1.0 op_sel:[0,1,0]
	v_pk_fma_f32 v[132:133], v[224:225], v[152:153], v[132:133] op_sel:[1,0,0] op_sel_hi:[1,1,1]
	v_cvt_scalef32_pk_f32_fp4 v[162:163], v26, 1.0 op_sel:[1,1,0]
	v_pk_fma_f32 v[134:135], v[224:225], v[154:155], v[134:135] op_sel:[1,0,0] op_sel_hi:[1,1,1]
	v_cvt_scalef32_pk_f32_fp4 v[152:153], v27, 1.0
	v_pk_fma_f32 v[136:137], v[224:225], v[156:157], v[136:137] op_sel:[1,0,0] op_sel_hi:[1,1,1]
	v_cvt_scalef32_pk_f32_fp4 v[154:155], v27, 1.0 op_sel:[1,0,0]
	v_pk_fma_f32 v[138:139], v[224:225], v[158:159], v[138:139] op_sel:[1,0,0] op_sel_hi:[1,1,1]
	v_cvt_scalef32_pk_f32_fp4 v[156:157], v27, 1.0 op_sel:[0,1,0]
	v_pk_fma_f32 v[140:141], v[224:225], v[160:161], v[140:141] op_sel:[1,0,0] op_sel_hi:[1,1,1]
	v_cvt_scalef32_pk_f32_fp4 v[158:159], v27, 1.0 op_sel:[1,1,0]
	v_pk_fma_f32 v[142:143], v[224:225], v[162:163], v[142:143] op_sel:[1,0,0] op_sel_hi:[1,1,1]
	v_pk_fma_f32 v[144:145], v[224:225], v[152:153], v[144:145] op_sel:[1,0,0] op_sel_hi:[1,1,1]
	v_pk_fma_f32 v[146:147], v[224:225], v[154:155], v[146:147] op_sel:[1,0,0] op_sel_hi:[1,1,1]
	v_pk_fma_f32 v[148:149], v[224:225], v[156:157], v[148:149] op_sel:[1,0,0] op_sel_hi:[1,1,1]
	v_pk_fma_f32 v[150:151], v[224:225], v[158:159], v[150:151] op_sel:[1,0,0] op_sel_hi:[1,1,1]
	v_cvt_scalef32_pk_f32_fp4 v[152:153], v20, 1.0
	v_cvt_scalef32_pk_f32_fp4 v[154:155], v20, 1.0 op_sel:[1,0,0]
	v_cvt_scalef32_pk_f32_fp4 v[156:157], v20, 1.0 op_sel:[0,1,0]
	v_cvt_scalef32_pk_f32_fp4 v[158:159], v20, 1.0 op_sel:[1,1,0]
	v_cvt_scalef32_pk_f32_fp4 v[160:161], v21, 1.0
	v_pk_fma_f32 v[120:121], v[226:227], v[152:153], v[120:121] op_sel_hi:[0,1,1]
	v_cvt_scalef32_pk_f32_fp4 v[162:163], v21, 1.0 op_sel:[1,0,0]
	v_pk_fma_f32 v[122:123], v[226:227], v[154:155], v[122:123] op_sel_hi:[0,1,1]
	v_cvt_scalef32_pk_f32_fp4 v[152:153], v21, 1.0 op_sel:[0,1,0]
	v_pk_fma_f32 v[124:125], v[226:227], v[156:157], v[124:125] op_sel_hi:[0,1,1]
	v_cvt_scalef32_pk_f32_fp4 v[154:155], v21, 1.0 op_sel:[1,1,0]
	v_pk_fma_f32 v[126:127], v[226:227], v[158:159], v[126:127] op_sel_hi:[0,1,1]
	v_cvt_scalef32_pk_f32_fp4 v[156:157], v22, 1.0
	v_pk_fma_f32 v[128:129], v[226:227], v[160:161], v[128:129] op_sel_hi:[0,1,1]
	v_cvt_scalef32_pk_f32_fp4 v[158:159], v22, 1.0 op_sel:[1,0,0]
	v_pk_fma_f32 v[130:131], v[226:227], v[162:163], v[130:131] op_sel_hi:[0,1,1]
	v_cvt_scalef32_pk_f32_fp4 v[160:161], v22, 1.0 op_sel:[0,1,0]
	v_pk_fma_f32 v[132:133], v[226:227], v[152:153], v[132:133] op_sel_hi:[0,1,1]
	v_cvt_scalef32_pk_f32_fp4 v[162:163], v22, 1.0 op_sel:[1,1,0]
	v_pk_fma_f32 v[134:135], v[226:227], v[154:155], v[134:135] op_sel_hi:[0,1,1]
	v_cvt_scalef32_pk_f32_fp4 v[152:153], v23, 1.0
	v_pk_fma_f32 v[136:137], v[226:227], v[156:157], v[136:137] op_sel_hi:[0,1,1]
	v_cvt_scalef32_pk_f32_fp4 v[154:155], v23, 1.0 op_sel:[1,0,0]
	v_pk_fma_f32 v[138:139], v[226:227], v[158:159], v[138:139] op_sel_hi:[0,1,1]
	v_cvt_scalef32_pk_f32_fp4 v[156:157], v23, 1.0 op_sel:[0,1,0]
	v_pk_fma_f32 v[140:141], v[226:227], v[160:161], v[140:141] op_sel_hi:[0,1,1]
	v_cvt_scalef32_pk_f32_fp4 v[158:159], v23, 1.0 op_sel:[1,1,0]
	v_pk_fma_f32 v[142:143], v[226:227], v[162:163], v[142:143] op_sel_hi:[0,1,1]
	v_pk_fma_f32 v[144:145], v[226:227], v[152:153], v[144:145] op_sel_hi:[0,1,1]
	v_pk_fma_f32 v[146:147], v[226:227], v[154:155], v[146:147] op_sel_hi:[0,1,1]
	v_pk_fma_f32 v[148:149], v[226:227], v[156:157], v[148:149] op_sel_hi:[0,1,1]
	v_pk_fma_f32 v[150:151], v[226:227], v[158:159], v[150:151] op_sel_hi:[0,1,1]
	v_cvt_scalef32_pk_f32_fp4 v[152:153], v16, 1.0
	v_cvt_scalef32_pk_f32_fp4 v[154:155], v16, 1.0 op_sel:[1,0,0]
	v_cvt_scalef32_pk_f32_fp4 v[156:157], v16, 1.0 op_sel:[0,1,0]
	v_cvt_scalef32_pk_f32_fp4 v[158:159], v16, 1.0 op_sel:[1,1,0]
	v_cvt_scalef32_pk_f32_fp4 v[160:161], v17, 1.0
	v_pk_fma_f32 v[120:121], v[226:227], v[152:153], v[120:121] op_sel:[1,0,0] op_sel_hi:[1,1,1]
	v_cvt_scalef32_pk_f32_fp4 v[162:163], v17, 1.0 op_sel:[1,0,0]
	v_pk_fma_f32 v[122:123], v[226:227], v[154:155], v[122:123] op_sel:[1,0,0] op_sel_hi:[1,1,1]
	v_cvt_scalef32_pk_f32_fp4 v[152:153], v17, 1.0 op_sel:[0,1,0]
	v_pk_fma_f32 v[124:125], v[226:227], v[156:157], v[124:125] op_sel:[1,0,0] op_sel_hi:[1,1,1]
	v_cvt_scalef32_pk_f32_fp4 v[154:155], v17, 1.0 op_sel:[1,1,0]
	v_pk_fma_f32 v[126:127], v[226:227], v[158:159], v[126:127] op_sel:[1,0,0] op_sel_hi:[1,1,1]
	v_cvt_scalef32_pk_f32_fp4 v[156:157], v18, 1.0
	v_pk_fma_f32 v[128:129], v[226:227], v[160:161], v[128:129] op_sel:[1,0,0] op_sel_hi:[1,1,1]
	v_cvt_scalef32_pk_f32_fp4 v[158:159], v18, 1.0 op_sel:[1,0,0]
	v_pk_fma_f32 v[130:131], v[226:227], v[162:163], v[130:131] op_sel:[1,0,0] op_sel_hi:[1,1,1]
	v_cvt_scalef32_pk_f32_fp4 v[160:161], v18, 1.0 op_sel:[0,1,0]
	v_pk_fma_f32 v[132:133], v[226:227], v[152:153], v[132:133] op_sel:[1,0,0] op_sel_hi:[1,1,1]
	v_cvt_scalef32_pk_f32_fp4 v[162:163], v18, 1.0 op_sel:[1,1,0]
	v_pk_fma_f32 v[134:135], v[226:227], v[154:155], v[134:135] op_sel:[1,0,0] op_sel_hi:[1,1,1]
	v_cvt_scalef32_pk_f32_fp4 v[152:153], v19, 1.0
	v_pk_fma_f32 v[136:137], v[226:227], v[156:157], v[136:137] op_sel:[1,0,0] op_sel_hi:[1,1,1]
	v_cvt_scalef32_pk_f32_fp4 v[154:155], v19, 1.0 op_sel:[1,0,0]
	v_pk_fma_f32 v[138:139], v[226:227], v[158:159], v[138:139] op_sel:[1,0,0] op_sel_hi:[1,1,1]
	v_cvt_scalef32_pk_f32_fp4 v[156:157], v19, 1.0 op_sel:[0,1,0]
	v_pk_fma_f32 v[140:141], v[226:227], v[160:161], v[140:141] op_sel:[1,0,0] op_sel_hi:[1,1,1]
	v_cvt_scalef32_pk_f32_fp4 v[158:159], v19, 1.0 op_sel:[1,1,0]
	v_pk_fma_f32 v[142:143], v[226:227], v[162:163], v[142:143] op_sel:[1,0,0] op_sel_hi:[1,1,1]
	v_pk_fma_f32 v[144:145], v[226:227], v[152:153], v[144:145] op_sel:[1,0,0] op_sel_hi:[1,1,1]
	v_pk_fma_f32 v[146:147], v[226:227], v[154:155], v[146:147] op_sel:[1,0,0] op_sel_hi:[1,1,1]
	v_pk_fma_f32 v[148:149], v[226:227], v[156:157], v[148:149] op_sel:[1,0,0] op_sel_hi:[1,1,1]
	v_pk_fma_f32 v[150:151], v[226:227], v[158:159], v[150:151] op_sel:[1,0,0] op_sel_hi:[1,1,1]
	v_cvt_scalef32_pk_f32_fp4 v[152:153], v12, 1.0
	v_cvt_scalef32_pk_f32_fp4 v[154:155], v12, 1.0 op_sel:[1,0,0]
	v_cvt_scalef32_pk_f32_fp4 v[156:157], v12, 1.0 op_sel:[0,1,0]
	v_cvt_scalef32_pk_f32_fp4 v[158:159], v12, 1.0 op_sel:[1,1,0]
	v_cvt_scalef32_pk_f32_fp4 v[160:161], v13, 1.0
	v_pk_fma_f32 v[120:121], v[228:229], v[152:153], v[120:121] op_sel_hi:[0,1,1]
	v_cvt_scalef32_pk_f32_fp4 v[162:163], v13, 1.0 op_sel:[1,0,0]
	v_pk_fma_f32 v[122:123], v[228:229], v[154:155], v[122:123] op_sel_hi:[0,1,1]
	v_cvt_scalef32_pk_f32_fp4 v[152:153], v13, 1.0 op_sel:[0,1,0]
	v_pk_fma_f32 v[124:125], v[228:229], v[156:157], v[124:125] op_sel_hi:[0,1,1]
	v_cvt_scalef32_pk_f32_fp4 v[154:155], v13, 1.0 op_sel:[1,1,0]
	v_pk_fma_f32 v[126:127], v[228:229], v[158:159], v[126:127] op_sel_hi:[0,1,1]
	v_cvt_scalef32_pk_f32_fp4 v[156:157], v14, 1.0
	v_pk_fma_f32 v[128:129], v[228:229], v[160:161], v[128:129] op_sel_hi:[0,1,1]
	v_cvt_scalef32_pk_f32_fp4 v[158:159], v14, 1.0 op_sel:[1,0,0]
	v_pk_fma_f32 v[130:131], v[228:229], v[162:163], v[130:131] op_sel_hi:[0,1,1]
	v_cvt_scalef32_pk_f32_fp4 v[160:161], v14, 1.0 op_sel:[0,1,0]
	v_pk_fma_f32 v[132:133], v[228:229], v[152:153], v[132:133] op_sel_hi:[0,1,1]
	v_cvt_scalef32_pk_f32_fp4 v[162:163], v14, 1.0 op_sel:[1,1,0]
	v_pk_fma_f32 v[134:135], v[228:229], v[154:155], v[134:135] op_sel_hi:[0,1,1]
	v_cvt_scalef32_pk_f32_fp4 v[152:153], v15, 1.0
	v_pk_fma_f32 v[136:137], v[228:229], v[156:157], v[136:137] op_sel_hi:[0,1,1]
	v_cvt_scalef32_pk_f32_fp4 v[154:155], v15, 1.0 op_sel:[1,0,0]
	v_pk_fma_f32 v[138:139], v[228:229], v[158:159], v[138:139] op_sel_hi:[0,1,1]
	v_cvt_scalef32_pk_f32_fp4 v[156:157], v15, 1.0 op_sel:[0,1,0]
	v_pk_fma_f32 v[140:141], v[228:229], v[160:161], v[140:141] op_sel_hi:[0,1,1]
	v_cvt_scalef32_pk_f32_fp4 v[158:159], v15, 1.0 op_sel:[1,1,0]
	v_pk_fma_f32 v[142:143], v[228:229], v[162:163], v[142:143] op_sel_hi:[0,1,1]
	v_pk_fma_f32 v[144:145], v[228:229], v[152:153], v[144:145] op_sel_hi:[0,1,1]
	v_pk_fma_f32 v[146:147], v[228:229], v[154:155], v[146:147] op_sel_hi:[0,1,1]
	v_pk_fma_f32 v[148:149], v[228:229], v[156:157], v[148:149] op_sel_hi:[0,1,1]
	v_pk_fma_f32 v[150:151], v[228:229], v[158:159], v[150:151] op_sel_hi:[0,1,1]
	v_cvt_scalef32_pk_f32_fp4 v[152:153], v8, 1.0
	v_cvt_scalef32_pk_f32_fp4 v[154:155], v8, 1.0 op_sel:[1,0,0]
	v_cvt_scalef32_pk_f32_fp4 v[156:157], v8, 1.0 op_sel:[0,1,0]
	v_cvt_scalef32_pk_f32_fp4 v[158:159], v8, 1.0 op_sel:[1,1,0]
	v_cvt_scalef32_pk_f32_fp4 v[160:161], v9, 1.0
	v_pk_fma_f32 v[120:121], v[228:229], v[152:153], v[120:121] op_sel:[1,0,0] op_sel_hi:[1,1,1]
	v_cvt_scalef32_pk_f32_fp4 v[162:163], v9, 1.0 op_sel:[1,0,0]
	v_pk_fma_f32 v[122:123], v[228:229], v[154:155], v[122:123] op_sel:[1,0,0] op_sel_hi:[1,1,1]
	v_cvt_scalef32_pk_f32_fp4 v[152:153], v9, 1.0 op_sel:[0,1,0]
	v_pk_fma_f32 v[124:125], v[228:229], v[156:157], v[124:125] op_sel:[1,0,0] op_sel_hi:[1,1,1]
	v_cvt_scalef32_pk_f32_fp4 v[154:155], v9, 1.0 op_sel:[1,1,0]
	v_pk_fma_f32 v[126:127], v[228:229], v[158:159], v[126:127] op_sel:[1,0,0] op_sel_hi:[1,1,1]
	v_cvt_scalef32_pk_f32_fp4 v[156:157], v10, 1.0
	v_pk_fma_f32 v[128:129], v[228:229], v[160:161], v[128:129] op_sel:[1,0,0] op_sel_hi:[1,1,1]
	v_cvt_scalef32_pk_f32_fp4 v[158:159], v10, 1.0 op_sel:[1,0,0]
	v_pk_fma_f32 v[130:131], v[228:229], v[162:163], v[130:131] op_sel:[1,0,0] op_sel_hi:[1,1,1]
	v_cvt_scalef32_pk_f32_fp4 v[160:161], v10, 1.0 op_sel:[0,1,0]
	v_pk_fma_f32 v[132:133], v[228:229], v[152:153], v[132:133] op_sel:[1,0,0] op_sel_hi:[1,1,1]
	v_cvt_scalef32_pk_f32_fp4 v[162:163], v10, 1.0 op_sel:[1,1,0]
	v_pk_fma_f32 v[134:135], v[228:229], v[154:155], v[134:135] op_sel:[1,0,0] op_sel_hi:[1,1,1]
	v_cvt_scalef32_pk_f32_fp4 v[152:153], v11, 1.0
	v_pk_fma_f32 v[136:137], v[228:229], v[156:157], v[136:137] op_sel:[1,0,0] op_sel_hi:[1,1,1]
	v_cvt_scalef32_pk_f32_fp4 v[154:155], v11, 1.0 op_sel:[1,0,0]
	v_pk_fma_f32 v[138:139], v[228:229], v[158:159], v[138:139] op_sel:[1,0,0] op_sel_hi:[1,1,1]
	v_cvt_scalef32_pk_f32_fp4 v[156:157], v11, 1.0 op_sel:[0,1,0]
	v_pk_fma_f32 v[140:141], v[228:229], v[160:161], v[140:141] op_sel:[1,0,0] op_sel_hi:[1,1,1]
	v_cvt_scalef32_pk_f32_fp4 v[158:159], v11, 1.0 op_sel:[1,1,0]
	v_pk_fma_f32 v[142:143], v[228:229], v[162:163], v[142:143] op_sel:[1,0,0] op_sel_hi:[1,1,1]
	v_pk_fma_f32 v[144:145], v[228:229], v[152:153], v[144:145] op_sel:[1,0,0] op_sel_hi:[1,1,1]
	v_pk_fma_f32 v[146:147], v[228:229], v[154:155], v[146:147] op_sel:[1,0,0] op_sel_hi:[1,1,1]
	v_pk_fma_f32 v[148:149], v[228:229], v[156:157], v[148:149] op_sel:[1,0,0] op_sel_hi:[1,1,1]
	v_pk_fma_f32 v[150:151], v[228:229], v[158:159], v[150:151] op_sel:[1,0,0] op_sel_hi:[1,1,1]
	v_cvt_scalef32_pk_f32_fp4 v[152:153], v4, 1.0
	v_cvt_scalef32_pk_f32_fp4 v[154:155], v4, 1.0 op_sel:[1,0,0]
	v_cvt_scalef32_pk_f32_fp4 v[156:157], v4, 1.0 op_sel:[0,1,0]
	v_cvt_scalef32_pk_f32_fp4 v[158:159], v4, 1.0 op_sel:[1,1,0]
	v_cvt_scalef32_pk_f32_fp4 v[160:161], v5, 1.0
	v_pk_fma_f32 v[120:121], v[230:231], v[152:153], v[120:121] op_sel_hi:[0,1,1]
	v_cvt_scalef32_pk_f32_fp4 v[162:163], v5, 1.0 op_sel:[1,0,0]
	v_pk_fma_f32 v[122:123], v[230:231], v[154:155], v[122:123] op_sel_hi:[0,1,1]
	v_cvt_scalef32_pk_f32_fp4 v[152:153], v5, 1.0 op_sel:[0,1,0]
	v_pk_fma_f32 v[124:125], v[230:231], v[156:157], v[124:125] op_sel_hi:[0,1,1]
	v_cvt_scalef32_pk_f32_fp4 v[154:155], v5, 1.0 op_sel:[1,1,0]
	v_pk_fma_f32 v[126:127], v[230:231], v[158:159], v[126:127] op_sel_hi:[0,1,1]
	v_cvt_scalef32_pk_f32_fp4 v[156:157], v6, 1.0
	v_pk_fma_f32 v[128:129], v[230:231], v[160:161], v[128:129] op_sel_hi:[0,1,1]
	v_cvt_scalef32_pk_f32_fp4 v[158:159], v6, 1.0 op_sel:[1,0,0]
	v_pk_fma_f32 v[130:131], v[230:231], v[162:163], v[130:131] op_sel_hi:[0,1,1]
	v_cvt_scalef32_pk_f32_fp4 v[160:161], v6, 1.0 op_sel:[0,1,0]
	v_pk_fma_f32 v[132:133], v[230:231], v[152:153], v[132:133] op_sel_hi:[0,1,1]
	v_cvt_scalef32_pk_f32_fp4 v[162:163], v6, 1.0 op_sel:[1,1,0]
	v_pk_fma_f32 v[134:135], v[230:231], v[154:155], v[134:135] op_sel_hi:[0,1,1]
	v_cvt_scalef32_pk_f32_fp4 v[152:153], v7, 1.0
	v_pk_fma_f32 v[136:137], v[230:231], v[156:157], v[136:137] op_sel_hi:[0,1,1]
	v_cvt_scalef32_pk_f32_fp4 v[154:155], v7, 1.0 op_sel:[1,0,0]
	v_pk_fma_f32 v[138:139], v[230:231], v[158:159], v[138:139] op_sel_hi:[0,1,1]
	v_cvt_scalef32_pk_f32_fp4 v[156:157], v7, 1.0 op_sel:[0,1,0]
	v_pk_fma_f32 v[140:141], v[230:231], v[160:161], v[140:141] op_sel_hi:[0,1,1]
	v_cvt_scalef32_pk_f32_fp4 v[158:159], v7, 1.0 op_sel:[1,1,0]
	v_pk_fma_f32 v[142:143], v[230:231], v[162:163], v[142:143] op_sel_hi:[0,1,1]
	v_pk_fma_f32 v[144:145], v[230:231], v[152:153], v[144:145] op_sel_hi:[0,1,1]
	v_pk_fma_f32 v[146:147], v[230:231], v[154:155], v[146:147] op_sel_hi:[0,1,1]
	v_pk_fma_f32 v[148:149], v[230:231], v[156:157], v[148:149] op_sel_hi:[0,1,1]
	v_pk_fma_f32 v[150:151], v[230:231], v[158:159], v[150:151] op_sel_hi:[0,1,1]
	v_cvt_scalef32_pk_f32_fp4 v[152:153], v0, 1.0
	v_cvt_scalef32_pk_f32_fp4 v[154:155], v0, 1.0 op_sel:[1,0,0]
	v_cvt_scalef32_pk_f32_fp4 v[156:157], v0, 1.0 op_sel:[0,1,0]
	v_cvt_scalef32_pk_f32_fp4 v[158:159], v0, 1.0 op_sel:[1,1,0]
	v_cvt_scalef32_pk_f32_fp4 v[160:161], v1, 1.0
	v_pk_fma_f32 v[120:121], v[230:231], v[152:153], v[120:121] op_sel:[1,0,0] op_sel_hi:[1,1,1]
	v_cvt_scalef32_pk_f32_fp4 v[162:163], v1, 1.0 op_sel:[1,0,0]
	v_pk_fma_f32 v[122:123], v[230:231], v[154:155], v[122:123] op_sel:[1,0,0] op_sel_hi:[1,1,1]
	v_cvt_scalef32_pk_f32_fp4 v[152:153], v1, 1.0 op_sel:[0,1,0]
	v_pk_fma_f32 v[124:125], v[230:231], v[156:157], v[124:125] op_sel:[1,0,0] op_sel_hi:[1,1,1]
	v_cvt_scalef32_pk_f32_fp4 v[154:155], v1, 1.0 op_sel:[1,1,0]
	v_pk_fma_f32 v[126:127], v[230:231], v[158:159], v[126:127] op_sel:[1,0,0] op_sel_hi:[1,1,1]
	v_cvt_scalef32_pk_f32_fp4 v[156:157], v2, 1.0
	v_pk_fma_f32 v[128:129], v[230:231], v[160:161], v[128:129] op_sel:[1,0,0] op_sel_hi:[1,1,1]
	v_cvt_scalef32_pk_f32_fp4 v[158:159], v2, 1.0 op_sel:[1,0,0]
	v_pk_fma_f32 v[130:131], v[230:231], v[162:163], v[130:131] op_sel:[1,0,0] op_sel_hi:[1,1,1]
	v_cvt_scalef32_pk_f32_fp4 v[160:161], v2, 1.0 op_sel:[0,1,0]
	v_pk_fma_f32 v[132:133], v[230:231], v[152:153], v[132:133] op_sel:[1,0,0] op_sel_hi:[1,1,1]
	v_cvt_scalef32_pk_f32_fp4 v[162:163], v2, 1.0 op_sel:[1,1,0]
	v_pk_fma_f32 v[134:135], v[230:231], v[154:155], v[134:135] op_sel:[1,0,0] op_sel_hi:[1,1,1]
	v_cvt_scalef32_pk_f32_fp4 v[152:153], v3, 1.0
	v_pk_fma_f32 v[136:137], v[230:231], v[156:157], v[136:137] op_sel:[1,0,0] op_sel_hi:[1,1,1]
	v_cvt_scalef32_pk_f32_fp4 v[154:155], v3, 1.0 op_sel:[1,0,0]
	v_pk_fma_f32 v[138:139], v[230:231], v[158:159], v[138:139] op_sel:[1,0,0] op_sel_hi:[1,1,1]
	v_cvt_scalef32_pk_f32_fp4 v[156:157], v3, 1.0 op_sel:[0,1,0]
	v_pk_fma_f32 v[140:141], v[230:231], v[160:161], v[140:141] op_sel:[1,0,0] op_sel_hi:[1,1,1]
	v_cvt_scalef32_pk_f32_fp4 v[158:159], v3, 1.0 op_sel:[1,1,0]
	v_pk_fma_f32 v[142:143], v[230:231], v[162:163], v[142:143] op_sel:[1,0,0] op_sel_hi:[1,1,1]
	v_pk_fma_f32 v[144:145], v[230:231], v[152:153], v[144:145] op_sel:[1,0,0] op_sel_hi:[1,1,1]
	v_pk_fma_f32 v[146:147], v[230:231], v[154:155], v[146:147] op_sel:[1,0,0] op_sel_hi:[1,1,1]
	v_pk_fma_f32 v[148:149], v[230:231], v[156:157], v[148:149] op_sel:[1,0,0] op_sel_hi:[1,1,1]
; __device__ void phase_exp_v(KParams& p, char* smem) {
;     ...
;         {
;           float* red = reinterpret_cast<float*>(smem + 8192) + w * 2304;
;           float* mr = red + (sub * 8 + cc) * 36;
; #pragma unroll
;           for (int q4 = 0; q4 < 8; ++q4)
;             *reinterpret_cast<float4*>(mr + q4 * 4) = float4{acc[q4 * 2].x, acc[q4 * 2].y, acc[q4 * 2 + 1].x, acc[q4 * 2 + 1].y};
;           __builtin_amdgcn_wave_barrier();
;           float4 r = *reinterpret_cast<const float4*>(red + (0 * 8 + sub) * 36 + cc * 4);
; #pragma unroll
;           for (int s8 = 1; s8 < 8; ++s8) {
;             const float4 r1 = *reinterpret_cast<const float4*>(red + (s8 * 8 + sub) * 36 + cc * 4);
;             r.x += r1.x; r.y += r1.y; r.z += r1.z; r.w += r1.w;
;           }
;           uint2 o4;
;           o4.x = pack2(r.x, r.y);
;           o4.y = pack2(r.z, r.w);
;           *reinterpret_cast<uint2*>(yfb + (size_t)t * D + x * 256 + sub * 32 + cc * 4) = o4;
	v_pk_fma_f32 v[150:151], v[230:231], v[158:159], v[150:151] op_sel:[1,0,0] op_sel_hi:[1,1,1]
	v_and_b32_e32 v170, 8, v44
	s_nop 0
	v_permlane32_swap_b32_e32 v120, v136
	v_permlane32_swap_b32_e32 v121, v137
	v_permlane32_swap_b32_e32 v122, v138
	v_permlane32_swap_b32_e32 v123, v139
	v_permlane32_swap_b32_e32 v124, v140
	v_permlane32_swap_b32_e32 v125, v141
	v_permlane32_swap_b32_e32 v126, v142
	v_permlane32_swap_b32_e32 v127, v143
	v_permlane32_swap_b32_e32 v128, v144
	v_permlane32_swap_b32_e32 v129, v145
	v_permlane32_swap_b32_e32 v130, v146
	v_permlane32_swap_b32_e32 v131, v147
	v_permlane32_swap_b32_e32 v132, v148
	v_permlane32_swap_b32_e32 v133, v149
	v_permlane32_swap_b32_e32 v134, v150
	v_permlane32_swap_b32_e32 v135, v151
	v_pk_add_f32 v[120:121], v[120:121], v[136:137]
	v_pk_add_f32 v[122:123], v[122:123], v[138:139]
	v_pk_add_f32 v[124:125], v[124:125], v[140:141]
	v_pk_add_f32 v[126:127], v[126:127], v[142:143]
	v_pk_add_f32 v[128:129], v[128:129], v[144:145]
	v_pk_add_f32 v[130:131], v[130:131], v[146:147]
	v_pk_add_f32 v[132:133], v[132:133], v[148:149]
	v_pk_add_f32 v[134:135], v[134:135], v[150:151]
	v_cmp_ne_u32_e32 vcc, 0, v170
	s_nop 0
	v_permlane16_swap_b32_e32 v120, v128
	v_permlane16_swap_b32_e32 v121, v129
	v_permlane16_swap_b32_e32 v122, v130
	v_permlane16_swap_b32_e32 v123, v131
	v_permlane16_swap_b32_e32 v124, v132
	v_permlane16_swap_b32_e32 v125, v133
	v_permlane16_swap_b32_e32 v126, v134
	v_permlane16_swap_b32_e32 v127, v135
	v_pk_add_f32 v[120:121], v[120:121], v[128:129]
	v_pk_add_f32 v[122:123], v[122:123], v[130:131]
	v_pk_add_f32 v[124:125], v[124:125], v[132:133]
	v_pk_add_f32 v[126:127], v[126:127], v[134:135]
	s_nop 1
	v_add_f32_dpp v136, v120, v120 row_ror:8 row_mask:0xf bank_mask:0xf
	v_add_f32_dpp v137, v121, v121 row_ror:8 row_mask:0xf bank_mask:0xf
	v_add_f32_dpp v138, v122, v122 row_ror:8 row_mask:0xf bank_mask:0xf
	v_add_f32_dpp v139, v123, v123 row_ror:8 row_mask:0xf bank_mask:0xf
	v_add_f32_dpp v140, v124, v124 row_ror:8 row_mask:0xf bank_mask:0xf
	v_add_f32_dpp v141, v125, v125 row_ror:8 row_mask:0xf bank_mask:0xf
	v_add_f32_dpp v142, v126, v126 row_ror:8 row_mask:0xf bank_mask:0xf
	v_add_f32_dpp v143, v127, v127 row_ror:8 row_mask:0xf bank_mask:0xf
	v_cndmask_b32_e32 v136, v136, v140, vcc
	v_cndmask_b32_e32 v137, v137, v141, vcc
	v_cndmask_b32_e32 v138, v138, v142, vcc
	v_cndmask_b32_e32 v139, v139, v143, vcc
	v_cvt_pk_bf16_f32 v176, v136, v137
	v_cvt_pk_bf16_f32 v177, v138, v139
	v_lshl_add_u64 v[118:119], v[52:53], 0, s[18:19]
	s_add_u32 s18, s18, 0x1000
	v_add_co_u32_e32 v118, vcc, s14, v118
	s_addc_u32 s19, s19, 0
	s_nop 0
	v_addc_co_u32_e32 v119, vcc, 0, v119, vcc
	global_store_dwordx2 v[118:119], v[176:177], off
	ds_read2_b32 v[216:217], v56 offset0:144 offset1:152
	ds_read2_b32 v[218:219], v56 offset0:160 offset1:168
	ds_read2_b32 v[220:221], v56 offset0:176 offset1:184
	ds_read2_b32 v[222:223], v56 offset0:192 offset1:200
	ds_read2_b32 v[224:225], v56 offset0:208 offset1:216
	ds_read2_b32 v[226:227], v56 offset0:224 offset1:232
	ds_read2_b32 v[228:229], v56 offset0:240 offset1:248
	ds_read2_b32 v[230:231], v61 offset1:8
	s_waitcnt lgkmcnt(0)
	s_waitcnt vmcnt(19)
	v_cvt_scalef32_pk_f32_fp4 v[152:153], v90, 1.0
	v_cvt_scalef32_pk_f32_fp4 v[154:155], v90, 1.0 op_sel:[1,0,0]
	v_cvt_scalef32_pk_f32_fp4 v[156:157], v90, 1.0 op_sel:[0,1,0]
	v_cvt_scalef32_pk_f32_fp4 v[158:159], v90, 1.0 op_sel:[1,1,0]
	v_cvt_scalef32_pk_f32_fp4 v[160:161], v91, 1.0
	v_pk_mul_f32 v[120:121], v[216:217], v[152:153] op_sel_hi:[0,1]
	v_cvt_scalef32_pk_f32_fp4 v[162:163], v91, 1.0 op_sel:[1,0,0]
	v_pk_mul_f32 v[122:123], v[216:217], v[154:155] op_sel_hi:[0,1]
	v_cvt_scalef32_pk_f32_fp4 v[152:153], v91, 1.0 op_sel:[0,1,0]
	v_pk_mul_f32 v[124:125], v[216:217], v[156:157] op_sel_hi:[0,1]
	v_cvt_scalef32_pk_f32_fp4 v[154:155], v91, 1.0 op_sel:[1,1,0]
	v_pk_mul_f32 v[126:127], v[216:217], v[158:159] op_sel_hi:[0,1]
	v_cvt_scalef32_pk_f32_fp4 v[156:157], v92, 1.0
	v_pk_mul_f32 v[128:129], v[216:217], v[160:161] op_sel_hi:[0,1]
	v_cvt_scalef32_pk_f32_fp4 v[158:159], v92, 1.0 op_sel:[1,0,0]
	v_pk_mul_f32 v[130:131], v[216:217], v[162:163] op_sel_hi:[0,1]
	v_cvt_scalef32_pk_f32_fp4 v[160:161], v92, 1.0 op_sel:[0,1,0]
	v_pk_mul_f32 v[132:133], v[216:217], v[152:153] op_sel_hi:[0,1]
	v_cvt_scalef32_pk_f32_fp4 v[162:163], v92, 1.0 op_sel:[1,1,0]
	v_pk_mul_f32 v[134:135], v[216:217], v[154:155] op_sel_hi:[0,1]
	v_cvt_scalef32_pk_f32_fp4 v[152:153], v93, 1.0
	v_pk_mul_f32 v[136:137], v[216:217], v[156:157] op_sel_hi:[0,1]
	v_cvt_scalef32_pk_f32_fp4 v[154:155], v93, 1.0 op_sel:[1,0,0]
	v_pk_mul_f32 v[138:139], v[216:217], v[158:159] op_sel_hi:[0,1]
	v_cvt_scalef32_pk_f32_fp4 v[156:157], v93, 1.0 op_sel:[0,1,0]
	v_pk_mul_f32 v[140:141], v[216:217], v[160:161] op_sel_hi:[0,1]
	v_cvt_scalef32_pk_f32_fp4 v[158:159], v93, 1.0 op_sel:[1,1,0]
	v_pk_mul_f32 v[142:143], v[216:217], v[162:163] op_sel_hi:[0,1]
	v_pk_mul_f32 v[144:145], v[216:217], v[152:153] op_sel_hi:[0,1]
	v_pk_mul_f32 v[146:147], v[216:217], v[154:155] op_sel_hi:[0,1]
	v_pk_mul_f32 v[148:149], v[216:217], v[156:157] op_sel_hi:[0,1]
	v_pk_mul_f32 v[150:151], v[216:217], v[158:159] op_sel_hi:[0,1]
	s_waitcnt vmcnt(18)
	v_cvt_scalef32_pk_f32_fp4 v[152:153], v94, 1.0
	v_cvt_scalef32_pk_f32_fp4 v[154:155], v94, 1.0 op_sel:[1,0,0]
	v_cvt_scalef32_pk_f32_fp4 v[156:157], v94, 1.0 op_sel:[0,1,0]
	v_cvt_scalef32_pk_f32_fp4 v[158:159], v94, 1.0 op_sel:[1,1,0]
	v_cvt_scalef32_pk_f32_fp4 v[160:161], v95, 1.0
	v_pk_fma_f32 v[120:121], v[216:217], v[152:153], v[120:121] op_sel:[1,0,0] op_sel_hi:[1,1,1]
	v_cvt_scalef32_pk_f32_fp4 v[162:163], v95, 1.0 op_sel:[1,0,0]
	v_pk_fma_f32 v[122:123], v[216:217], v[154:155], v[122:123] op_sel:[1,0,0] op_sel_hi:[1,1,1]
	v_cvt_scalef32_pk_f32_fp4 v[152:153], v95, 1.0 op_sel:[0,1,0]
	v_pk_fma_f32 v[124:125], v[216:217], v[156:157], v[124:125] op_sel:[1,0,0] op_sel_hi:[1,1,1]
	v_cvt_scalef32_pk_f32_fp4 v[154:155], v95, 1.0 op_sel:[1,1,0]
	v_pk_fma_f32 v[126:127], v[216:217], v[158:159], v[126:127] op_sel:[1,0,0] op_sel_hi:[1,1,1]
	v_cvt_scalef32_pk_f32_fp4 v[156:157], v96, 1.0
	v_pk_fma_f32 v[128:129], v[216:217], v[160:161], v[128:129] op_sel:[1,0,0] op_sel_hi:[1,1,1]
	v_cvt_scalef32_pk_f32_fp4 v[158:159], v96, 1.0 op_sel:[1,0,0]
	v_pk_fma_f32 v[130:131], v[216:217], v[162:163], v[130:131] op_sel:[1,0,0] op_sel_hi:[1,1,1]
	v_cvt_scalef32_pk_f32_fp4 v[160:161], v96, 1.0 op_sel:[0,1,0]
	v_pk_fma_f32 v[132:133], v[216:217], v[152:153], v[132:133] op_sel:[1,0,0] op_sel_hi:[1,1,1]
	v_cvt_scalef32_pk_f32_fp4 v[162:163], v96, 1.0 op_sel:[1,1,0]
	v_pk_fma_f32 v[134:135], v[216:217], v[154:155], v[134:135] op_sel:[1,0,0] op_sel_hi:[1,1,1]
	v_cvt_scalef32_pk_f32_fp4 v[152:153], v97, 1.0
	v_pk_fma_f32 v[136:137], v[216:217], v[156:157], v[136:137] op_sel:[1,0,0] op_sel_hi:[1,1,1]
	v_cvt_scalef32_pk_f32_fp4 v[154:155], v97, 1.0 op_sel:[1,0,0]
	v_pk_fma_f32 v[138:139], v[216:217], v[158:159], v[138:139] op_sel:[1,0,0] op_sel_hi:[1,1,1]
	v_cvt_scalef32_pk_f32_fp4 v[156:157], v97, 1.0 op_sel:[0,1,0]
	v_pk_fma_f32 v[140:141], v[216:217], v[160:161], v[140:141] op_sel:[1,0,0] op_sel_hi:[1,1,1]
	v_cvt_scalef32_pk_f32_fp4 v[158:159], v97, 1.0 op_sel:[1,1,0]
	v_pk_fma_f32 v[142:143], v[216:217], v[162:163], v[142:143] op_sel:[1,0,0] op_sel_hi:[1,1,1]
	v_pk_fma_f32 v[144:145], v[216:217], v[152:153], v[144:145] op_sel:[1,0,0] op_sel_hi:[1,1,1]
	v_pk_fma_f32 v[146:147], v[216:217], v[154:155], v[146:147] op_sel:[1,0,0] op_sel_hi:[1,1,1]
	v_pk_fma_f32 v[148:149], v[216:217], v[156:157], v[148:149] op_sel:[1,0,0] op_sel_hi:[1,1,1]
	v_pk_fma_f32 v[150:151], v[216:217], v[158:159], v[150:151] op_sel:[1,0,0] op_sel_hi:[1,1,1]
	s_waitcnt vmcnt(17)
	v_cvt_scalef32_pk_f32_fp4 v[152:153], v98, 1.0
	v_cvt_scalef32_pk_f32_fp4 v[154:155], v98, 1.0 op_sel:[1,0,0]
	v_cvt_scalef32_pk_f32_fp4 v[156:157], v98, 1.0 op_sel:[0,1,0]
	v_cvt_scalef32_pk_f32_fp4 v[158:159], v98, 1.0 op_sel:[1,1,0]
	v_cvt_scalef32_pk_f32_fp4 v[160:161], v99, 1.0
	v_pk_fma_f32 v[120:121], v[218:219], v[152:153], v[120:121] op_sel_hi:[0,1,1]
	v_cvt_scalef32_pk_f32_fp4 v[162:163], v99, 1.0 op_sel:[1,0,0]
	v_pk_fma_f32 v[122:123], v[218:219], v[154:155], v[122:123] op_sel_hi:[0,1,1]
	v_cvt_scalef32_pk_f32_fp4 v[152:153], v99, 1.0 op_sel:[0,1,0]
	v_pk_fma_f32 v[124:125], v[218:219], v[156:157], v[124:125] op_sel_hi:[0,1,1]
	v_cvt_scalef32_pk_f32_fp4 v[154:155], v99, 1.0 op_sel:[1,1,0]
	v_pk_fma_f32 v[126:127], v[218:219], v[158:159], v[126:127] op_sel_hi:[0,1,1]
	v_cvt_scalef32_pk_f32_fp4 v[156:157], v100, 1.0
	v_pk_fma_f32 v[128:129], v[218:219], v[160:161], v[128:129] op_sel_hi:[0,1,1]
	v_cvt_scalef32_pk_f32_fp4 v[158:159], v100, 1.0 op_sel:[1,0,0]
	v_pk_fma_f32 v[130:131], v[218:219], v[162:163], v[130:131] op_sel_hi:[0,1,1]
	v_cvt_scalef32_pk_f32_fp4 v[160:161], v100, 1.0 op_sel:[0,1,0]
	v_pk_fma_f32 v[132:133], v[218:219], v[152:153], v[132:133] op_sel_hi:[0,1,1]
	v_cvt_scalef32_pk_f32_fp4 v[162:163], v100, 1.0 op_sel:[1,1,0]
	v_pk_fma_f32 v[134:135], v[218:219], v[154:155], v[134:135] op_sel_hi:[0,1,1]
	v_cvt_scalef32_pk_f32_fp4 v[152:153], v101, 1.0
	v_pk_fma_f32 v[136:137], v[218:219], v[156:157], v[136:137] op_sel_hi:[0,1,1]
	v_cvt_scalef32_pk_f32_fp4 v[154:155], v101, 1.0 op_sel:[1,0,0]
	v_pk_fma_f32 v[138:139], v[218:219], v[158:159], v[138:139] op_sel_hi:[0,1,1]
	v_cvt_scalef32_pk_f32_fp4 v[156:157], v101, 1.0 op_sel:[0,1,0]
	v_pk_fma_f32 v[140:141], v[218:219], v[160:161], v[140:141] op_sel_hi:[0,1,1]
	v_cvt_scalef32_pk_f32_fp4 v[158:159], v101, 1.0 op_sel:[1,1,0]
	v_pk_fma_f32 v[142:143], v[218:219], v[162:163], v[142:143] op_sel_hi:[0,1,1]
	v_pk_fma_f32 v[144:145], v[218:219], v[152:153], v[144:145] op_sel_hi:[0,1,1]
	v_pk_fma_f32 v[146:147], v[218:219], v[154:155], v[146:147] op_sel_hi:[0,1,1]
	v_pk_fma_f32 v[148:149], v[218:219], v[156:157], v[148:149] op_sel_hi:[0,1,1]
	v_pk_fma_f32 v[150:151], v[218:219], v[158:159], v[150:151] op_sel_hi:[0,1,1]
	s_waitcnt vmcnt(16)
; #define EV_LOADN(q_, g0_, n_) _Pragma("unroll") for (int k = 0; k < (n_); ++k) q_[k] = __builtin_bit_cast(uint4, __builtin_amdgcn_raw_buffer_load_b128(vrs, voff + si[((g0_) + k) * 8 + sub] * 128, 0, GATHER_AUX))
; __device__ void phase_exp_v(KParams& p, char* smem) {
;     ...
;         EV_LOADN(qa, 0, 4); EV_LOADN(qb, 4, 4); EV_LOADN(qc, 8, 4); EV_LOADN(qd, 12, 4);
;         {
;           const int t1 = (tt + 1 < 16) ? t + 1 : t;
;           e0n = p.idx[(size_t)t1 * 128 + lane]; e1n = p.idx[(size_t)t1 * 128 + 64 + lane];
;           g0n = p.gate[(size_t)t1 * 128 + lane]; g1n = p.gate[(size_t)t1 * 128 + 64 + lane];
;         }
	v_cvt_scalef32_pk_f32_fp4 v[152:153], v102, 1.0
	v_cvt_scalef32_pk_f32_fp4 v[154:155], v102, 1.0 op_sel:[1,0,0]
	v_cvt_scalef32_pk_f32_fp4 v[156:157], v102, 1.0 op_sel:[0,1,0]
	v_cvt_scalef32_pk_f32_fp4 v[158:159], v102, 1.0 op_sel:[1,1,0]
	v_cvt_scalef32_pk_f32_fp4 v[160:161], v103, 1.0
	v_pk_fma_f32 v[120:121], v[218:219], v[152:153], v[120:121] op_sel:[1,0,0] op_sel_hi:[1,1,1]
	v_cvt_scalef32_pk_f32_fp4 v[162:163], v103, 1.0 op_sel:[1,0,0]
	v_pk_fma_f32 v[122:123], v[218:219], v[154:155], v[122:123] op_sel:[1,0,0] op_sel_hi:[1,1,1]
	v_cvt_scalef32_pk_f32_fp4 v[152:153], v103, 1.0 op_sel:[0,1,0]
	v_pk_fma_f32 v[124:125], v[218:219], v[156:157], v[124:125] op_sel:[1,0,0] op_sel_hi:[1,1,1]
	v_cvt_scalef32_pk_f32_fp4 v[154:155], v103, 1.0 op_sel:[1,1,0]
	v_pk_fma_f32 v[126:127], v[218:219], v[158:159], v[126:127] op_sel:[1,0,0] op_sel_hi:[1,1,1]
	v_cvt_scalef32_pk_f32_fp4 v[156:157], v104, 1.0
	v_pk_fma_f32 v[128:129], v[218:219], v[160:161], v[128:129] op_sel:[1,0,0] op_sel_hi:[1,1,1]
	v_cvt_scalef32_pk_f32_fp4 v[158:159], v104, 1.0 op_sel:[1,0,0]
	v_pk_fma_f32 v[130:131], v[218:219], v[162:163], v[130:131] op_sel:[1,0,0] op_sel_hi:[1,1,1]
	v_cvt_scalef32_pk_f32_fp4 v[160:161], v104, 1.0 op_sel:[0,1,0]
	v_pk_fma_f32 v[132:133], v[218:219], v[152:153], v[132:133] op_sel:[1,0,0] op_sel_hi:[1,1,1]
	v_cvt_scalef32_pk_f32_fp4 v[162:163], v104, 1.0 op_sel:[1,1,0]
	v_pk_fma_f32 v[134:135], v[218:219], v[154:155], v[134:135] op_sel:[1,0,0] op_sel_hi:[1,1,1]
	v_cvt_scalef32_pk_f32_fp4 v[152:153], v105, 1.0
	v_pk_fma_f32 v[136:137], v[218:219], v[156:157], v[136:137] op_sel:[1,0,0] op_sel_hi:[1,1,1]
	v_cvt_scalef32_pk_f32_fp4 v[154:155], v105, 1.0 op_sel:[1,0,0]
	v_pk_fma_f32 v[138:139], v[218:219], v[158:159], v[138:139] op_sel:[1,0,0] op_sel_hi:[1,1,1]
	v_cvt_scalef32_pk_f32_fp4 v[156:157], v105, 1.0 op_sel:[0,1,0]
	v_pk_fma_f32 v[140:141], v[218:219], v[160:161], v[140:141] op_sel:[1,0,0] op_sel_hi:[1,1,1]
	v_cvt_scalef32_pk_f32_fp4 v[158:159], v105, 1.0 op_sel:[1,1,0]
	v_pk_fma_f32 v[142:143], v[218:219], v[162:163], v[142:143] op_sel:[1,0,0] op_sel_hi:[1,1,1]
	v_pk_fma_f32 v[144:145], v[218:219], v[152:153], v[144:145] op_sel:[1,0,0] op_sel_hi:[1,1,1]
	v_pk_fma_f32 v[146:147], v[218:219], v[154:155], v[146:147] op_sel:[1,0,0] op_sel_hi:[1,1,1]
	v_pk_fma_f32 v[148:149], v[218:219], v[156:157], v[148:149] op_sel:[1,0,0] op_sel_hi:[1,1,1]
	v_pk_fma_f32 v[150:151], v[218:219], v[158:159], v[150:151] op_sel:[1,0,0] op_sel_hi:[1,1,1]
	s_waitcnt vmcnt(0)
	s_cmpk_eq_u32 s18, 0xf000
	s_cbranch_scc1 .Lmy_ev_nopf_b
	ds_write2_b32 v54, v64, v65 offset0:16 offset1:80
	ds_write2_b32 v54, v66, v67 offset0:144 offset1:208
	ds_read2_b32 v[200:201], v56 offset0:16 offset1:24
	ds_read2_b32 v[202:203], v56 offset0:32 offset1:40
	ds_read2_b32 v[204:205], v56 offset0:48 offset1:56
	ds_read2_b32 v[206:207], v56 offset0:64 offset1:72
	ds_read2_b32 v[208:209], v56 offset0:80 offset1:88
	ds_read2_b32 v[210:211], v56 offset0:96 offset1:104
	ds_read2_b32 v[212:213], v56 offset0:112 offset1:120
	ds_read2_b32 v[214:215], v56 offset0:128 offset1:136
	s_cmpk_lg_u32 s18, 0xe000
	s_cselect_b64 s[20:21], -1, 0
	v_cndmask_b32_e64 v64, 0, 1, s[20:21]
	v_mov_b32_e32 v65, s37
	v_lshl_add_u64 v[64:65], v[50:51], 0, v[64:65]
	v_lshlrev_b64 v[66:67], 9, v[64:65]
	v_mov_b32_e32 v50, v64
	v_mov_b32_e32 v51, v65
	v_lshl_or_b32 v66, v44, 2, v66
	v_lshl_add_u64 v[88:89], s[10:11], 0, v[66:67]
	s_waitcnt lgkmcnt(7)
	v_lshl_add_u32 v168, v200, 7, v63
	buffer_load_dwordx4 v[68:71], v168, s[12:15], 0 offen sc0
	v_lshl_add_u32 v168, v201, 7, v63
	buffer_load_dwordx4 v[72:75], v168, s[12:15], 0 offen sc0
	s_waitcnt lgkmcnt(6)
	v_lshl_add_u32 v168, v202, 7, v63
	buffer_load_dwordx4 v[76:79], v168, s[12:15], 0 offen sc0
	v_lshl_add_u32 v168, v203, 7, v63
	buffer_load_dwordx4 v[80:83], v168, s[12:15], 0 offen sc0
	s_waitcnt lgkmcnt(5)
	v_lshl_add_u32 v168, v204, 7, v63
	buffer_load_dwordx4 v[84:87], v168, s[12:15], 0 offen sc0
	v_lshl_add_u32 v168, v205, 7, v63
	buffer_load_dwordx4 v[40:43], v168, s[12:15], 0 offen sc0
	s_waitcnt lgkmcnt(4)
	v_lshl_add_u32 v168, v206, 7, v63
	buffer_load_dwordx4 v[36:39], v168, s[12:15], 0 offen sc0
	v_lshl_add_u32 v168, v207, 7, v63
	buffer_load_dwordx4 v[32:35], v168, s[12:15], 0 offen sc0
	s_waitcnt lgkmcnt(3)
	v_lshl_add_u32 v168, v208, 7, v63
	buffer_load_dwordx4 v[28:31], v168, s[12:15], 0 offen sc0
	v_lshl_add_u32 v168, v209, 7, v63
	buffer_load_dwordx4 v[24:27], v168, s[12:15], 0 offen sc0
	s_waitcnt lgkmcnt(2)
	v_lshl_add_u32 v168, v210, 7, v63
	buffer_load_dwordx4 v[20:23], v168, s[12:15], 0 offen sc0
	v_lshl_add_u32 v168, v211, 7, v63
	buffer_load_dwordx4 v[16:19], v168, s[12:15], 0 offen sc0
	s_waitcnt lgkmcnt(1)
	v_lshl_add_u32 v168, v212, 7, v63
	buffer_load_dwordx4 v[12:15], v168, s[12:15], 0 offen sc0
	v_lshl_add_u32 v168, v213, 7, v63
	buffer_load_dwordx4 v[8:11], v168, s[12:15], 0 offen sc0
	s_waitcnt lgkmcnt(0)
	v_lshl_add_u32 v168, v214, 7, v63
	buffer_load_dwordx4 v[4:7], v168, s[12:15], 0 offen sc0
	v_lshl_add_u32 v168, v215, 7, v63
	buffer_load_dwordx4 v[0:3], v168, s[12:15], 0 offen sc0
	s_nop 0
	global_load_dword v64, v[88:89], off
	global_load_dword v65, v[88:89], off offset:256
	v_lshl_add_u64 v[88:89], s[8:9], 0, v[66:67]
	global_load_dword v66, v[88:89], off
	global_load_dword v67, v[88:89], off offset:256
.Lmy_ev_nopf_b:
	v_cvt_scalef32_pk_f32_fp4 v[152:153], v106, 1.0
	v_cvt_scalef32_pk_f32_fp4 v[154:155], v106, 1.0 op_sel:[1,0,0]
	v_cvt_scalef32_pk_f32_fp4 v[156:157], v106, 1.0 op_sel:[0,1,0]
	v_cvt_scalef32_pk_f32_fp4 v[158:159], v106, 1.0 op_sel:[1,1,0]
	v_cvt_scalef32_pk_f32_fp4 v[160:161], v107, 1.0
	v_pk_fma_f32 v[120:121], v[220:221], v[152:153], v[120:121] op_sel_hi:[0,1,1]
	v_cvt_scalef32_pk_f32_fp4 v[162:163], v107, 1.0 op_sel:[1,0,0]
	v_pk_fma_f32 v[122:123], v[220:221], v[154:155], v[122:123] op_sel_hi:[0,1,1]
	v_cvt_scalef32_pk_f32_fp4 v[152:153], v107, 1.0 op_sel:[0,1,0]
	v_pk_fma_f32 v[124:125], v[220:221], v[156:157], v[124:125] op_sel_hi:[0,1,1]
	v_cvt_scalef32_pk_f32_fp4 v[154:155], v107, 1.0 op_sel:[1,1,0]
	v_pk_fma_f32 v[126:127], v[220:221], v[158:159], v[126:127] op_sel_hi:[0,1,1]
	v_cvt_scalef32_pk_f32_fp4 v[156:157], v108, 1.0
	v_pk_fma_f32 v[128:129], v[220:221], v[160:161], v[128:129] op_sel_hi:[0,1,1]
	v_cvt_scalef32_pk_f32_fp4 v[158:159], v108, 1.0 op_sel:[1,0,0]
	v_pk_fma_f32 v[130:131], v[220:221], v[162:163], v[130:131] op_sel_hi:[0,1,1]
	v_cvt_scalef32_pk_f32_fp4 v[160:161], v108, 1.0 op_sel:[0,1,0]
	v_pk_fma_f32 v[132:133], v[220:221], v[152:153], v[132:133] op_sel_hi:[0,1,1]
	v_cvt_scalef32_pk_f32_fp4 v[162:163], v108, 1.0 op_sel:[1,1,0]
	v_pk_fma_f32 v[134:135], v[220:221], v[154:155], v[134:135] op_sel_hi:[0,1,1]
	v_cvt_scalef32_pk_f32_fp4 v[152:153], v109, 1.0
	v_pk_fma_f32 v[136:137], v[220:221], v[156:157], v[136:137] op_sel_hi:[0,1,1]
	v_cvt_scalef32_pk_f32_fp4 v[154:155], v109, 1.0 op_sel:[1,0,0]
	v_pk_fma_f32 v[138:139], v[220:221], v[158:159], v[138:139] op_sel_hi:[0,1,1]
	v_cvt_scalef32_pk_f32_fp4 v[156:157], v109, 1.0 op_sel:[0,1,0]
	v_pk_fma_f32 v[140:141], v[220:221], v[160:161], v[140:141] op_sel_hi:[0,1,1]
	v_cvt_scalef32_pk_f32_fp4 v[158:159], v109, 1.0 op_sel:[1,1,0]
	v_pk_fma_f32 v[142:143], v[220:221], v[162:163], v[142:143] op_sel_hi:[0,1,1]
	v_pk_fma_f32 v[144:145], v[220:221], v[152:153], v[144:145] op_sel_hi:[0,1,1]
	v_pk_fma_f32 v[146:147], v[220:221], v[154:155], v[146:147] op_sel_hi:[0,1,1]
	v_pk_fma_f32 v[148:149], v[220:221], v[156:157], v[148:149] op_sel_hi:[0,1,1]
	v_pk_fma_f32 v[150:151], v[220:221], v[158:159], v[150:151] op_sel_hi:[0,1,1]
	v_cvt_scalef32_pk_f32_fp4 v[152:153], v110, 1.0
	v_cvt_scalef32_pk_f32_fp4 v[154:155], v110, 1.0 op_sel:[1,0,0]
	v_cvt_scalef32_pk_f32_fp4 v[156:157], v110, 1.0 op_sel:[0,1,0]
	v_cvt_scalef32_pk_f32_fp4 v[158:159], v110, 1.0 op_sel:[1,1,0]
	v_cvt_scalef32_pk_f32_fp4 v[160:161], v111, 1.0
	v_pk_fma_f32 v[120:121], v[220:221], v[152:153], v[120:121] op_sel:[1,0,0] op_sel_hi:[1,1,1]
	v_cvt_scalef32_pk_f32_fp4 v[162:163], v111, 1.0 op_sel:[1,0,0]
	v_pk_fma_f32 v[122:123], v[220:221], v[154:155], v[122:123] op_sel:[1,0,0] op_sel_hi:[1,1,1]
	v_cvt_scalef32_pk_f32_fp4 v[152:153], v111, 1.0 op_sel:[0,1,0]
	v_pk_fma_f32 v[124:125], v[220:221], v[156:157], v[124:125] op_sel:[1,0,0] op_sel_hi:[1,1,1]
	v_cvt_scalef32_pk_f32_fp4 v[154:155], v111, 1.0 op_sel:[1,1,0]
	v_pk_fma_f32 v[126:127], v[220:221], v[158:159], v[126:127] op_sel:[1,0,0] op_sel_hi:[1,1,1]
	v_cvt_scalef32_pk_f32_fp4 v[156:157], v112, 1.0
	v_pk_fma_f32 v[128:129], v[220:221], v[160:161], v[128:129] op_sel:[1,0,0] op_sel_hi:[1,1,1]
	v_cvt_scalef32_pk_f32_fp4 v[158:159], v112, 1.0 op_sel:[1,0,0]
	v_pk_fma_f32 v[130:131], v[220:221], v[162:163], v[130:131] op_sel:[1,0,0] op_sel_hi:[1,1,1]
	v_cvt_scalef32_pk_f32_fp4 v[160:161], v112, 1.0 op_sel:[0,1,0]
	v_pk_fma_f32 v[132:133], v[220:221], v[152:153], v[132:133] op_sel:[1,0,0] op_sel_hi:[1,1,1]
	v_cvt_scalef32_pk_f32_fp4 v[162:163], v112, 1.0 op_sel:[1,1,0]
	v_pk_fma_f32 v[134:135], v[220:221], v[154:155], v[134:135] op_sel:[1,0,0] op_sel_hi:[1,1,1]
	v_cvt_scalef32_pk_f32_fp4 v[152:153], v113, 1.0
	v_pk_fma_f32 v[136:137], v[220:221], v[156:157], v[136:137] op_sel:[1,0,0] op_sel_hi:[1,1,1]
	v_cvt_scalef32_pk_f32_fp4 v[154:155], v113, 1.0 op_sel:[1,0,0]
	v_pk_fma_f32 v[138:139], v[220:221], v[158:159], v[138:139] op_sel:[1,0,0] op_sel_hi:[1,1,1]
	v_cvt_scalef32_pk_f32_fp4 v[156:157], v113, 1.0 op_sel:[0,1,0]
	v_pk_fma_f32 v[140:141], v[220:221], v[160:161], v[140:141] op_sel:[1,0,0] op_sel_hi:[1,1,1]
	v_cvt_scalef32_pk_f32_fp4 v[158:159], v113, 1.0 op_sel:[1,1,0]
	v_pk_fma_f32 v[142:143], v[220:221], v[162:163], v[142:143] op_sel:[1,0,0] op_sel_hi:[1,1,1]
	v_pk_fma_f32 v[144:145], v[220:221], v[152:153], v[144:145] op_sel:[1,0,0] op_sel_hi:[1,1,1]
	v_pk_fma_f32 v[146:147], v[220:221], v[154:155], v[146:147] op_sel:[1,0,0] op_sel_hi:[1,1,1]
	v_pk_fma_f32 v[148:149], v[220:221], v[156:157], v[148:149] op_sel:[1,0,0] op_sel_hi:[1,1,1]
	v_pk_fma_f32 v[150:151], v[220:221], v[158:159], v[150:151] op_sel:[1,0,0] op_sel_hi:[1,1,1]
	v_cvt_scalef32_pk_f32_fp4 v[152:153], v114, 1.0
	v_cvt_scalef32_pk_f32_fp4 v[154:155], v114, 1.0 op_sel:[1,0,0]
	v_cvt_scalef32_pk_f32_fp4 v[156:157], v114, 1.0 op_sel:[0,1,0]
	v_cvt_scalef32_pk_f32_fp4 v[158:159], v114, 1.0 op_sel:[1,1,0]
	v_cvt_scalef32_pk_f32_fp4 v[160:161], v115, 1.0
	v_pk_fma_f32 v[120:121], v[222:223], v[152:153], v[120:121] op_sel_hi:[0,1,1]
	v_cvt_scalef32_pk_f32_fp4 v[162:163], v115, 1.0 op_sel:[1,0,0]
	v_pk_fma_f32 v[122:123], v[222:223], v[154:155], v[122:123] op_sel_hi:[0,1,1]
	v_cvt_scalef32_pk_f32_fp4 v[152:153], v115, 1.0 op_sel:[0,1,0]
	v_pk_fma_f32 v[124:125], v[222:223], v[156:157], v[124:125] op_sel_hi:[0,1,1]
	v_cvt_scalef32_pk_f32_fp4 v[154:155], v115, 1.0 op_sel:[1,1,0]
	v_pk_fma_f32 v[126:127], v[222:223], v[158:159], v[126:127] op_sel_hi:[0,1,1]
	v_cvt_scalef32_pk_f32_fp4 v[156:157], v116, 1.0
	v_pk_fma_f32 v[128:129], v[222:223], v[160:161], v[128:129] op_sel_hi:[0,1,1]
	v_cvt_scalef32_pk_f32_fp4 v[158:159], v116, 1.0 op_sel:[1,0,0]
	v_pk_fma_f32 v[130:131], v[222:223], v[162:163], v[130:131] op_sel_hi:[0,1,1]
	v_cvt_scalef32_pk_f32_fp4 v[160:161], v116, 1.0 op_sel:[0,1,0]
	v_pk_fma_f32 v[132:133], v[222:223], v[152:153], v[132:133] op_sel_hi:[0,1,1]
	v_cvt_scalef32_pk_f32_fp4 v[162:163], v116, 1.0 op_sel:[1,1,0]
	v_pk_fma_f32 v[134:135], v[222:223], v[154:155], v[134:135] op_sel_hi:[0,1,1]
	v_cvt_scalef32_pk_f32_fp4 v[152:153], v117, 1.0
	v_pk_fma_f32 v[136:137], v[222:223], v[156:157], v[136:137] op_sel_hi:[0,1,1]
	v_cvt_scalef32_pk_f32_fp4 v[154:155], v117, 1.0 op_sel:[1,0,0]
	v_pk_fma_f32 v[138:139], v[222:223], v[158:159], v[138:139] op_sel_hi:[0,1,1]
	v_cvt_scalef32_pk_f32_fp4 v[156:157], v117, 1.0 op_sel:[0,1,0]
	v_pk_fma_f32 v[140:141], v[222:223], v[160:161], v[140:141] op_sel_hi:[0,1,1]
	v_cvt_scalef32_pk_f32_fp4 v[158:159], v117, 1.0 op_sel:[1,1,0]
	v_pk_fma_f32 v[142:143], v[222:223], v[162:163], v[142:143] op_sel_hi:[0,1,1]
	v_pk_fma_f32 v[144:145], v[222:223], v[152:153], v[144:145] op_sel_hi:[0,1,1]
	v_pk_fma_f32 v[146:147], v[222:223], v[154:155], v[146:147] op_sel_hi:[0,1,1]
	v_pk_fma_f32 v[148:149], v[222:223], v[156:157], v[148:149] op_sel_hi:[0,1,1]
	v_pk_fma_f32 v[150:151], v[222:223], v[158:159], v[150:151] op_sel_hi:[0,1,1]
	v_cvt_scalef32_pk_f32_fp4 v[152:153], v232, 1.0
	v_cvt_scalef32_pk_f32_fp4 v[154:155], v232, 1.0 op_sel:[1,0,0]
	v_cvt_scalef32_pk_f32_fp4 v[156:157], v232, 1.0 op_sel:[0,1,0]
	v_cvt_scalef32_pk_f32_fp4 v[158:159], v232, 1.0 op_sel:[1,1,0]
	v_cvt_scalef32_pk_f32_fp4 v[160:161], v233, 1.0
	v_pk_fma_f32 v[120:121], v[222:223], v[152:153], v[120:121] op_sel:[1,0,0] op_sel_hi:[1,1,1]
	v_cvt_scalef32_pk_f32_fp4 v[162:163], v233, 1.0 op_sel:[1,0,0]
	v_pk_fma_f32 v[122:123], v[222:223], v[154:155], v[122:123] op_sel:[1,0,0] op_sel_hi:[1,1,1]
	v_cvt_scalef32_pk_f32_fp4 v[152:153], v233, 1.0 op_sel:[0,1,0]
	v_pk_fma_f32 v[124:125], v[222:223], v[156:157], v[124:125] op_sel:[1,0,0] op_sel_hi:[1,1,1]
	v_cvt_scalef32_pk_f32_fp4 v[154:155], v233, 1.0 op_sel:[1,1,0]
	v_pk_fma_f32 v[126:127], v[222:223], v[158:159], v[126:127] op_sel:[1,0,0] op_sel_hi:[1,1,1]
	v_cvt_scalef32_pk_f32_fp4 v[156:157], v234, 1.0
	v_pk_fma_f32 v[128:129], v[222:223], v[160:161], v[128:129] op_sel:[1,0,0] op_sel_hi:[1,1,1]
	v_cvt_scalef32_pk_f32_fp4 v[158:159], v234, 1.0 op_sel:[1,0,0]
	v_pk_fma_f32 v[130:131], v[222:223], v[162:163], v[130:131] op_sel:[1,0,0] op_sel_hi:[1,1,1]
	v_cvt_scalef32_pk_f32_fp4 v[160:161], v234, 1.0 op_sel:[0,1,0]
	v_pk_fma_f32 v[132:133], v[222:223], v[152:153], v[132:133] op_sel:[1,0,0] op_sel_hi:[1,1,1]
	v_cvt_scalef32_pk_f32_fp4 v[162:163], v234, 1.0 op_sel:[1,1,0]
	v_pk_fma_f32 v[134:135], v[222:223], v[154:155], v[134:135] op_sel:[1,0,0] op_sel_hi:[1,1,1]
	v_cvt_scalef32_pk_f32_fp4 v[152:153], v235, 1.0
	v_pk_fma_f32 v[136:137], v[222:223], v[156:157], v[136:137] op_sel:[1,0,0] op_sel_hi:[1,1,1]
	v_cvt_scalef32_pk_f32_fp4 v[154:155], v235, 1.0 op_sel:[1,0,0]
	v_pk_fma_f32 v[138:139], v[222:223], v[158:159], v[138:139] op_sel:[1,0,0] op_sel_hi:[1,1,1]
	v_cvt_scalef32_pk_f32_fp4 v[156:157], v235, 1.0 op_sel:[0,1,0]
	v_pk_fma_f32 v[140:141], v[222:223], v[160:161], v[140:141] op_sel:[1,0,0] op_sel_hi:[1,1,1]
	v_cvt_scalef32_pk_f32_fp4 v[158:159], v235, 1.0 op_sel:[1,1,0]
	v_pk_fma_f32 v[142:143], v[222:223], v[162:163], v[142:143] op_sel:[1,0,0] op_sel_hi:[1,1,1]
	v_pk_fma_f32 v[144:145], v[222:223], v[152:153], v[144:145] op_sel:[1,0,0] op_sel_hi:[1,1,1]
	v_pk_fma_f32 v[146:147], v[222:223], v[154:155], v[146:147] op_sel:[1,0,0] op_sel_hi:[1,1,1]
	v_pk_fma_f32 v[148:149], v[222:223], v[156:157], v[148:149] op_sel:[1,0,0] op_sel_hi:[1,1,1]
	v_pk_fma_f32 v[150:151], v[222:223], v[158:159], v[150:151] op_sel:[1,0,0] op_sel_hi:[1,1,1]
	v_cvt_scalef32_pk_f32_fp4 v[152:153], v236, 1.0
	v_cvt_scalef32_pk_f32_fp4 v[154:155], v236, 1.0 op_sel:[1,0,0]
	v_cvt_scalef32_pk_f32_fp4 v[156:157], v236, 1.0 op_sel:[0,1,0]
	v_cvt_scalef32_pk_f32_fp4 v[158:159], v236, 1.0 op_sel:[1,1,0]
	v_cvt_scalef32_pk_f32_fp4 v[160:161], v237, 1.0
	v_pk_fma_f32 v[120:121], v[224:225], v[152:153], v[120:121] op_sel_hi:[0,1,1]
	v_cvt_scalef32_pk_f32_fp4 v[162:163], v237, 1.0 op_sel:[1,0,0]
	v_pk_fma_f32 v[122:123], v[224:225], v[154:155], v[122:123] op_sel_hi:[0,1,1]
	v_cvt_scalef32_pk_f32_fp4 v[152:153], v237, 1.0 op_sel:[0,1,0]
	v_pk_fma_f32 v[124:125], v[224:225], v[156:157], v[124:125] op_sel_hi:[0,1,1]
	v_cvt_scalef32_pk_f32_fp4 v[154:155], v237, 1.0 op_sel:[1,1,0]
	v_pk_fma_f32 v[126:127], v[224:225], v[158:159], v[126:127] op_sel_hi:[0,1,1]
	v_cvt_scalef32_pk_f32_fp4 v[156:157], v238, 1.0
	v_pk_fma_f32 v[128:129], v[224:225], v[160:161], v[128:129] op_sel_hi:[0,1,1]
	v_cvt_scalef32_pk_f32_fp4 v[158:159], v238, 1.0 op_sel:[1,0,0]
	v_pk_fma_f32 v[130:131], v[224:225], v[162:163], v[130:131] op_sel_hi:[0,1,1]
	v_cvt_scalef32_pk_f32_fp4 v[160:161], v238, 1.0 op_sel:[0,1,0]
	v_pk_fma_f32 v[132:133], v[224:225], v[152:153], v[132:133] op_sel_hi:[0,1,1]
	v_cvt_scalef32_pk_f32_fp4 v[162:163], v238, 1.0 op_sel:[1,1,0]
	v_pk_fma_f32 v[134:135], v[224:225], v[154:155], v[134:135] op_sel_hi:[0,1,1]
	v_cvt_scalef32_pk_f32_fp4 v[152:153], v239, 1.0
	v_pk_fma_f32 v[136:137], v[224:225], v[156:157], v[136:137] op_sel_hi:[0,1,1]
	v_cvt_scalef32_pk_f32_fp4 v[154:155], v239, 1.0 op_sel:[1,0,0]
	v_pk_fma_f32 v[138:139], v[224:225], v[158:159], v[138:139] op_sel_hi:[0,1,1]
	v_cvt_scalef32_pk_f32_fp4 v[156:157], v239, 1.0 op_sel:[0,1,0]
	v_pk_fma_f32 v[140:141], v[224:225], v[160:161], v[140:141] op_sel_hi:[0,1,1]
	v_cvt_scalef32_pk_f32_fp4 v[158:159], v239, 1.0 op_sel:[1,1,0]
	v_pk_fma_f32 v[142:143], v[224:225], v[162:163], v[142:143] op_sel_hi:[0,1,1]
	v_pk_fma_f32 v[144:145], v[224:225], v[152:153], v[144:145] op_sel_hi:[0,1,1]
	v_pk_fma_f32 v[146:147], v[224:225], v[154:155], v[146:147] op_sel_hi:[0,1,1]
	v_pk_fma_f32 v[148:149], v[224:225], v[156:157], v[148:149] op_sel_hi:[0,1,1]
	v_pk_fma_f32 v[150:151], v[224:225], v[158:159], v[150:151] op_sel_hi:[0,1,1]
	v_cvt_scalef32_pk_f32_fp4 v[152:153], v240, 1.0
	v_cvt_scalef32_pk_f32_fp4 v[154:155], v240, 1.0 op_sel:[1,0,0]
	v_cvt_scalef32_pk_f32_fp4 v[156:157], v240, 1.0 op_sel:[0,1,0]
	v_cvt_scalef32_pk_f32_fp4 v[158:159], v240, 1.0 op_sel:[1,1,0]
	v_cvt_scalef32_pk_f32_fp4 v[160:161], v241, 1.0
	v_pk_fma_f32 v[120:121], v[224:225], v[152:153], v[120:121] op_sel:[1,0,0] op_sel_hi:[1,1,1]
	v_cvt_scalef32_pk_f32_fp4 v[162:163], v241, 1.0 op_sel:[1,0,0]
	v_pk_fma_f32 v[122:123], v[224:225], v[154:155], v[122:123] op_sel:[1,0,0] op_sel_hi:[1,1,1]
	v_cvt_scalef32_pk_f32_fp4 v[152:153], v241, 1.0 op_sel:[0,1,0]
	v_pk_fma_f32 v[124:125], v[224:225], v[156:157], v[124:125] op_sel:[1,0,0] op_sel_hi:[1,1,1]
	v_cvt_scalef32_pk_f32_fp4 v[154:155], v241, 1.0 op_sel:[1,1,0]
	v_pk_fma_f32 v[126:127], v[224:225], v[158:159], v[126:127] op_sel:[1,0,0] op_sel_hi:[1,1,1]
	v_cvt_scalef32_pk_f32_fp4 v[156:157], v242, 1.0
	v_pk_fma_f32 v[128:129], v[224:225], v[160:161], v[128:129] op_sel:[1,0,0] op_sel_hi:[1,1,1]
	v_cvt_scalef32_pk_f32_fp4 v[158:159], v242, 1.0 op_sel:[1,0,0]
	v_pk_fma_f32 v[130:131], v[224:225], v[162:163], v[130:131] op_sel:[1,0,0] op_sel_hi:[1,1,1]
	v_cvt_scalef32_pk_f32_fp4 v[160:161], v242, 1.0 op_sel:[0,1,0]
	v_pk_fma_f32 v[132:133], v[224:225], v[152:153], v[132:133] op_sel:[1,0,0] op_sel_hi:[1,1,1]
	v_cvt_scalef32_pk_f32_fp4 v[162:163], v242, 1.0 op_sel:[1,1,0]
	v_pk_fma_f32 v[134:135], v[224:225], v[154:155], v[134:135] op_sel:[1,0,0] op_sel_hi:[1,1,1]
	v_cvt_scalef32_pk_f32_fp4 v[152:153], v243, 1.0
	v_pk_fma_f32 v[136:137], v[224:225], v[156:157], v[136:137] op_sel:[1,0,0] op_sel_hi:[1,1,1]
	v_cvt_scalef32_pk_f32_fp4 v[154:155], v243, 1.0 op_sel:[1,0,0]
	v_pk_fma_f32 v[138:139], v[224:225], v[158:159], v[138:139] op_sel:[1,0,0] op_sel_hi:[1,1,1]
	v_cvt_scalef32_pk_f32_fp4 v[156:157], v243, 1.0 op_sel:[0,1,0]
	v_pk_fma_f32 v[140:141], v[224:225], v[160:161], v[140:141] op_sel:[1,0,0] op_sel_hi:[1,1,1]
	v_cvt_scalef32_pk_f32_fp4 v[158:159], v243, 1.0 op_sel:[1,1,0]
	v_pk_fma_f32 v[142:143], v[224:225], v[162:163], v[142:143] op_sel:[1,0,0] op_sel_hi:[1,1,1]
	v_pk_fma_f32 v[144:145], v[224:225], v[152:153], v[144:145] op_sel:[1,0,0] op_sel_hi:[1,1,1]
	v_pk_fma_f32 v[146:147], v[224:225], v[154:155], v[146:147] op_sel:[1,0,0] op_sel_hi:[1,1,1]
	v_pk_fma_f32 v[148:149], v[224:225], v[156:157], v[148:149] op_sel:[1,0,0] op_sel_hi:[1,1,1]
	v_pk_fma_f32 v[150:151], v[224:225], v[158:159], v[150:151] op_sel:[1,0,0] op_sel_hi:[1,1,1]
	v_cvt_scalef32_pk_f32_fp4 v[152:153], v244, 1.0
	v_cvt_scalef32_pk_f32_fp4 v[154:155], v244, 1.0 op_sel:[1,0,0]
	v_cvt_scalef32_pk_f32_fp4 v[156:157], v244, 1.0 op_sel:[0,1,0]
	v_cvt_scalef32_pk_f32_fp4 v[158:159], v244, 1.0 op_sel:[1,1,0]
	v_cvt_scalef32_pk_f32_fp4 v[160:161], v245, 1.0
	v_pk_fma_f32 v[120:121], v[226:227], v[152:153], v[120:121] op_sel_hi:[0,1,1]
	v_cvt_scalef32_pk_f32_fp4 v[162:163], v245, 1.0 op_sel:[1,0,0]
	v_pk_fma_f32 v[122:123], v[226:227], v[154:155], v[122:123] op_sel_hi:[0,1,1]
	v_cvt_scalef32_pk_f32_fp4 v[152:153], v245, 1.0 op_sel:[0,1,0]
	v_pk_fma_f32 v[124:125], v[226:227], v[156:157], v[124:125] op_sel_hi:[0,1,1]
	v_cvt_scalef32_pk_f32_fp4 v[154:155], v245, 1.0 op_sel:[1,1,0]
	v_pk_fma_f32 v[126:127], v[226:227], v[158:159], v[126:127] op_sel_hi:[0,1,1]
	v_cvt_scalef32_pk_f32_fp4 v[156:157], v246, 1.0
	v_pk_fma_f32 v[128:129], v[226:227], v[160:161], v[128:129] op_sel_hi:[0,1,1]
	v_cvt_scalef32_pk_f32_fp4 v[158:159], v246, 1.0 op_sel:[1,0,0]
	v_pk_fma_f32 v[130:131], v[226:227], v[162:163], v[130:131] op_sel_hi:[0,1,1]
	v_cvt_scalef32_pk_f32_fp4 v[160:161], v246, 1.0 op_sel:[0,1,0]
	v_pk_fma_f32 v[132:133], v[226:227], v[152:153], v[132:133] op_sel_hi:[0,1,1]
	v_cvt_scalef32_pk_f32_fp4 v[162:163], v246, 1.0 op_sel:[1,1,0]
	v_pk_fma_f32 v[134:135], v[226:227], v[154:155], v[134:135] op_sel_hi:[0,1,1]
	v_cvt_scalef32_pk_f32_fp4 v[152:153], v247, 1.0
	v_pk_fma_f32 v[136:137], v[226:227], v[156:157], v[136:137] op_sel_hi:[0,1,1]
	v_cvt_scalef32_pk_f32_fp4 v[154:155], v247, 1.0 op_sel:[1,0,0]
	v_pk_fma_f32 v[138:139], v[226:227], v[158:159], v[138:139] op_sel_hi:[0,1,1]
	v_cvt_scalef32_pk_f32_fp4 v[156:157], v247, 1.0 op_sel:[0,1,0]
	v_pk_fma_f32 v[140:141], v[226:227], v[160:161], v[140:141] op_sel_hi:[0,1,1]
	v_cvt_scalef32_pk_f32_fp4 v[158:159], v247, 1.0 op_sel:[1,1,0]
	v_pk_fma_f32 v[142:143], v[226:227], v[162:163], v[142:143] op_sel_hi:[0,1,1]
	v_pk_fma_f32 v[144:145], v[226:227], v[152:153], v[144:145] op_sel_hi:[0,1,1]
	v_pk_fma_f32 v[146:147], v[226:227], v[154:155], v[146:147] op_sel_hi:[0,1,1]
	v_pk_fma_f32 v[148:149], v[226:227], v[156:157], v[148:149] op_sel_hi:[0,1,1]
	v_pk_fma_f32 v[150:151], v[226:227], v[158:159], v[150:151] op_sel_hi:[0,1,1]
	v_cvt_scalef32_pk_f32_fp4 v[152:153], v248, 1.0
	v_cvt_scalef32_pk_f32_fp4 v[154:155], v248, 1.0 op_sel:[1,0,0]
	v_cvt_scalef32_pk_f32_fp4 v[156:157], v248, 1.0 op_sel:[0,1,0]
	v_cvt_scalef32_pk_f32_fp4 v[158:159], v248, 1.0 op_sel:[1,1,0]
	v_cvt_scalef32_pk_f32_fp4 v[160:161], v249, 1.0
	v_pk_fma_f32 v[120:121], v[226:227], v[152:153], v[120:121] op_sel:[1,0,0] op_sel_hi:[1,1,1]
	v_cvt_scalef32_pk_f32_fp4 v[162:163], v249, 1.0 op_sel:[1,0,0]
	v_pk_fma_f32 v[122:123], v[226:227], v[154:155], v[122:123] op_sel:[1,0,0] op_sel_hi:[1,1,1]
	v_cvt_scalef32_pk_f32_fp4 v[152:153], v249, 1.0 op_sel:[0,1,0]
	v_pk_fma_f32 v[124:125], v[226:227], v[156:157], v[124:125] op_sel:[1,0,0] op_sel_hi:[1,1,1]
	v_cvt_scalef32_pk_f32_fp4 v[154:155], v249, 1.0 op_sel:[1,1,0]
	v_pk_fma_f32 v[126:127], v[226:227], v[158:159], v[126:127] op_sel:[1,0,0] op_sel_hi:[1,1,1]
	v_cvt_scalef32_pk_f32_fp4 v[156:157], v250, 1.0
	v_pk_fma_f32 v[128:129], v[226:227], v[160:161], v[128:129] op_sel:[1,0,0] op_sel_hi:[1,1,1]
	v_cvt_scalef32_pk_f32_fp4 v[158:159], v250, 1.0 op_sel:[1,0,0]
	v_pk_fma_f32 v[130:131], v[226:227], v[162:163], v[130:131] op_sel:[1,0,0] op_sel_hi:[1,1,1]
	v_cvt_scalef32_pk_f32_fp4 v[160:161], v250, 1.0 op_sel:[0,1,0]
	v_pk_fma_f32 v[132:133], v[226:227], v[152:153], v[132:133] op_sel:[1,0,0] op_sel_hi:[1,1,1]
	v_cvt_scalef32_pk_f32_fp4 v[162:163], v250, 1.0 op_sel:[1,1,0]
	v_pk_fma_f32 v[134:135], v[226:227], v[154:155], v[134:135] op_sel:[1,0,0] op_sel_hi:[1,1,1]
	v_cvt_scalef32_pk_f32_fp4 v[152:153], v251, 1.0
	v_pk_fma_f32 v[136:137], v[226:227], v[156:157], v[136:137] op_sel:[1,0,0] op_sel_hi:[1,1,1]
	v_cvt_scalef32_pk_f32_fp4 v[154:155], v251, 1.0 op_sel:[1,0,0]
	v_pk_fma_f32 v[138:139], v[226:227], v[158:159], v[138:139] op_sel:[1,0,0] op_sel_hi:[1,1,1]
	v_cvt_scalef32_pk_f32_fp4 v[156:157], v251, 1.0 op_sel:[0,1,0]
	v_pk_fma_f32 v[140:141], v[226:227], v[160:161], v[140:141] op_sel:[1,0,0] op_sel_hi:[1,1,1]
	v_cvt_scalef32_pk_f32_fp4 v[158:159], v251, 1.0 op_sel:[1,1,0]
	v_pk_fma_f32 v[142:143], v[226:227], v[162:163], v[142:143] op_sel:[1,0,0] op_sel_hi:[1,1,1]
	v_pk_fma_f32 v[144:145], v[226:227], v[152:153], v[144:145] op_sel:[1,0,0] op_sel_hi:[1,1,1]
	v_pk_fma_f32 v[146:147], v[226:227], v[154:155], v[146:147] op_sel:[1,0,0] op_sel_hi:[1,1,1]
	v_pk_fma_f32 v[148:149], v[226:227], v[156:157], v[148:149] op_sel:[1,0,0] op_sel_hi:[1,1,1]
	v_pk_fma_f32 v[150:151], v[226:227], v[158:159], v[150:151] op_sel:[1,0,0] op_sel_hi:[1,1,1]
	v_cvt_scalef32_pk_f32_fp4 v[152:153], v164, 1.0
	v_cvt_scalef32_pk_f32_fp4 v[154:155], v164, 1.0 op_sel:[1,0,0]
	v_cvt_scalef32_pk_f32_fp4 v[156:157], v164, 1.0 op_sel:[0,1,0]
	v_cvt_scalef32_pk_f32_fp4 v[158:159], v164, 1.0 op_sel:[1,1,0]
	v_cvt_scalef32_pk_f32_fp4 v[160:161], v165, 1.0
	v_pk_fma_f32 v[120:121], v[228:229], v[152:153], v[120:121] op_sel_hi:[0,1,1]
	v_cvt_scalef32_pk_f32_fp4 v[162:163], v165, 1.0 op_sel:[1,0,0]
	v_pk_fma_f32 v[122:123], v[228:229], v[154:155], v[122:123] op_sel_hi:[0,1,1]
	v_cvt_scalef32_pk_f32_fp4 v[152:153], v165, 1.0 op_sel:[0,1,0]
	v_pk_fma_f32 v[124:125], v[228:229], v[156:157], v[124:125] op_sel_hi:[0,1,1]
	v_cvt_scalef32_pk_f32_fp4 v[154:155], v165, 1.0 op_sel:[1,1,0]
	v_pk_fma_f32 v[126:127], v[228:229], v[158:159], v[126:127] op_sel_hi:[0,1,1]
	v_cvt_scalef32_pk_f32_fp4 v[156:157], v166, 1.0
	v_pk_fma_f32 v[128:129], v[228:229], v[160:161], v[128:129] op_sel_hi:[0,1,1]
	v_cvt_scalef32_pk_f32_fp4 v[158:159], v166, 1.0 op_sel:[1,0,0]
	v_pk_fma_f32 v[130:131], v[228:229], v[162:163], v[130:131] op_sel_hi:[0,1,1]
	v_cvt_scalef32_pk_f32_fp4 v[160:161], v166, 1.0 op_sel:[0,1,0]
	v_pk_fma_f32 v[132:133], v[228:229], v[152:153], v[132:133] op_sel_hi:[0,1,1]
	v_cvt_scalef32_pk_f32_fp4 v[162:163], v166, 1.0 op_sel:[1,1,0]
	v_pk_fma_f32 v[134:135], v[228:229], v[154:155], v[134:135] op_sel_hi:[0,1,1]
	v_cvt_scalef32_pk_f32_fp4 v[152:153], v167, 1.0
	v_pk_fma_f32 v[136:137], v[228:229], v[156:157], v[136:137] op_sel_hi:[0,1,1]
	v_cvt_scalef32_pk_f32_fp4 v[154:155], v167, 1.0 op_sel:[1,0,0]
	v_pk_fma_f32 v[138:139], v[228:229], v[158:159], v[138:139] op_sel_hi:[0,1,1]
	v_cvt_scalef32_pk_f32_fp4 v[156:157], v167, 1.0 op_sel:[0,1,0]
	v_pk_fma_f32 v[140:141], v[228:229], v[160:161], v[140:141] op_sel_hi:[0,1,1]
	v_cvt_scalef32_pk_f32_fp4 v[158:159], v167, 1.0 op_sel:[1,1,0]
	v_pk_fma_f32 v[142:143], v[228:229], v[162:163], v[142:143] op_sel_hi:[0,1,1]
	v_pk_fma_f32 v[144:145], v[228:229], v[152:153], v[144:145] op_sel_hi:[0,1,1]
	v_pk_fma_f32 v[146:147], v[228:229], v[154:155], v[146:147] op_sel_hi:[0,1,1]
	v_pk_fma_f32 v[148:149], v[228:229], v[156:157], v[148:149] op_sel_hi:[0,1,1]
	v_pk_fma_f32 v[150:151], v[228:229], v[158:159], v[150:151] op_sel_hi:[0,1,1]
	v_cvt_scalef32_pk_f32_fp4 v[152:153], v172, 1.0
	v_cvt_scalef32_pk_f32_fp4 v[154:155], v172, 1.0 op_sel:[1,0,0]
	v_cvt_scalef32_pk_f32_fp4 v[156:157], v172, 1.0 op_sel:[0,1,0]
	v_cvt_scalef32_pk_f32_fp4 v[158:159], v172, 1.0 op_sel:[1,1,0]
	v_cvt_scalef32_pk_f32_fp4 v[160:161], v173, 1.0
	v_pk_fma_f32 v[120:121], v[228:229], v[152:153], v[120:121] op_sel:[1,0,0] op_sel_hi:[1,1,1]
	v_cvt_scalef32_pk_f32_fp4 v[162:163], v173, 1.0 op_sel:[1,0,0]
	v_pk_fma_f32 v[122:123], v[228:229], v[154:155], v[122:123] op_sel:[1,0,0] op_sel_hi:[1,1,1]
	v_cvt_scalef32_pk_f32_fp4 v[152:153], v173, 1.0 op_sel:[0,1,0]
	v_pk_fma_f32 v[124:125], v[228:229], v[156:157], v[124:125] op_sel:[1,0,0] op_sel_hi:[1,1,1]
	v_cvt_scalef32_pk_f32_fp4 v[154:155], v173, 1.0 op_sel:[1,1,0]
	v_pk_fma_f32 v[126:127], v[228:229], v[158:159], v[126:127] op_sel:[1,0,0] op_sel_hi:[1,1,1]
	v_cvt_scalef32_pk_f32_fp4 v[156:157], v174, 1.0
	v_pk_fma_f32 v[128:129], v[228:229], v[160:161], v[128:129] op_sel:[1,0,0] op_sel_hi:[1,1,1]
	v_cvt_scalef32_pk_f32_fp4 v[158:159], v174, 1.0 op_sel:[1,0,0]
	v_pk_fma_f32 v[130:131], v[228:229], v[162:163], v[130:131] op_sel:[1,0,0] op_sel_hi:[1,1,1]
	v_cvt_scalef32_pk_f32_fp4 v[160:161], v174, 1.0 op_sel:[0,1,0]
	v_pk_fma_f32 v[132:133], v[228:229], v[152:153], v[132:133] op_sel:[1,0,0] op_sel_hi:[1,1,1]
	v_cvt_scalef32_pk_f32_fp4 v[162:163], v174, 1.0 op_sel:[1,1,0]
	v_pk_fma_f32 v[134:135], v[228:229], v[154:155], v[134:135] op_sel:[1,0,0] op_sel_hi:[1,1,1]
	v_cvt_scalef32_pk_f32_fp4 v[152:153], v175, 1.0
	v_pk_fma_f32 v[136:137], v[228:229], v[156:157], v[136:137] op_sel:[1,0,0] op_sel_hi:[1,1,1]
	v_cvt_scalef32_pk_f32_fp4 v[154:155], v175, 1.0 op_sel:[1,0,0]
	v_pk_fma_f32 v[138:139], v[228:229], v[158:159], v[138:139] op_sel:[1,0,0] op_sel_hi:[1,1,1]
	v_cvt_scalef32_pk_f32_fp4 v[156:157], v175, 1.0 op_sel:[0,1,0]
	v_pk_fma_f32 v[140:141], v[228:229], v[160:161], v[140:141] op_sel:[1,0,0] op_sel_hi:[1,1,1]
	v_cvt_scalef32_pk_f32_fp4 v[158:159], v175, 1.0 op_sel:[1,1,0]
	v_pk_fma_f32 v[142:143], v[228:229], v[162:163], v[142:143] op_sel:[1,0,0] op_sel_hi:[1,1,1]
	v_pk_fma_f32 v[144:145], v[228:229], v[152:153], v[144:145] op_sel:[1,0,0] op_sel_hi:[1,1,1]
	v_pk_fma_f32 v[146:147], v[228:229], v[154:155], v[146:147] op_sel:[1,0,0] op_sel_hi:[1,1,1]
	v_pk_fma_f32 v[148:149], v[228:229], v[156:157], v[148:149] op_sel:[1,0,0] op_sel_hi:[1,1,1]
	v_pk_fma_f32 v[150:151], v[228:229], v[158:159], v[150:151] op_sel:[1,0,0] op_sel_hi:[1,1,1]
	v_cvt_scalef32_pk_f32_fp4 v[152:153], v192, 1.0
	v_cvt_scalef32_pk_f32_fp4 v[154:155], v192, 1.0 op_sel:[1,0,0]
	v_cvt_scalef32_pk_f32_fp4 v[156:157], v192, 1.0 op_sel:[0,1,0]
	v_cvt_scalef32_pk_f32_fp4 v[158:159], v192, 1.0 op_sel:[1,1,0]
	v_cvt_scalef32_pk_f32_fp4 v[160:161], v193, 1.0
	v_pk_fma_f32 v[120:121], v[230:231], v[152:153], v[120:121] op_sel_hi:[0,1,1]
	v_cvt_scalef32_pk_f32_fp4 v[162:163], v193, 1.0 op_sel:[1,0,0]
	v_pk_fma_f32 v[122:123], v[230:231], v[154:155], v[122:123] op_sel_hi:[0,1,1]
	v_cvt_scalef32_pk_f32_fp4 v[152:153], v193, 1.0 op_sel:[0,1,0]
	v_pk_fma_f32 v[124:125], v[230:231], v[156:157], v[124:125] op_sel_hi:[0,1,1]
	v_cvt_scalef32_pk_f32_fp4 v[154:155], v193, 1.0 op_sel:[1,1,0]
	v_pk_fma_f32 v[126:127], v[230:231], v[158:159], v[126:127] op_sel_hi:[0,1,1]
	v_cvt_scalef32_pk_f32_fp4 v[156:157], v194, 1.0
	v_pk_fma_f32 v[128:129], v[230:231], v[160:161], v[128:129] op_sel_hi:[0,1,1]
	v_cvt_scalef32_pk_f32_fp4 v[158:159], v194, 1.0 op_sel:[1,0,0]
	v_pk_fma_f32 v[130:131], v[230:231], v[162:163], v[130:131] op_sel_hi:[0,1,1]
	v_cvt_scalef32_pk_f32_fp4 v[160:161], v194, 1.0 op_sel:[0,1,0]
	v_pk_fma_f32 v[132:133], v[230:231], v[152:153], v[132:133] op_sel_hi:[0,1,1]
	v_cvt_scalef32_pk_f32_fp4 v[162:163], v194, 1.0 op_sel:[1,1,0]
	v_pk_fma_f32 v[134:135], v[230:231], v[154:155], v[134:135] op_sel_hi:[0,1,1]
	v_cvt_scalef32_pk_f32_fp4 v[152:153], v195, 1.0
	v_pk_fma_f32 v[136:137], v[230:231], v[156:157], v[136:137] op_sel_hi:[0,1,1]
	v_cvt_scalef32_pk_f32_fp4 v[154:155], v195, 1.0 op_sel:[1,0,0]
	v_pk_fma_f32 v[138:139], v[230:231], v[158:159], v[138:139] op_sel_hi:[0,1,1]
	v_cvt_scalef32_pk_f32_fp4 v[156:157], v195, 1.0 op_sel:[0,1,0]
	v_pk_fma_f32 v[140:141], v[230:231], v[160:161], v[140:141] op_sel_hi:[0,1,1]
	v_cvt_scalef32_pk_f32_fp4 v[158:159], v195, 1.0 op_sel:[1,1,0]
	v_pk_fma_f32 v[142:143], v[230:231], v[162:163], v[142:143] op_sel_hi:[0,1,1]
	v_pk_fma_f32 v[144:145], v[230:231], v[152:153], v[144:145] op_sel_hi:[0,1,1]
	v_pk_fma_f32 v[146:147], v[230:231], v[154:155], v[146:147] op_sel_hi:[0,1,1]
	v_pk_fma_f32 v[148:149], v[230:231], v[156:157], v[148:149] op_sel_hi:[0,1,1]
	v_pk_fma_f32 v[150:151], v[230:231], v[158:159], v[150:151] op_sel_hi:[0,1,1]
	v_cvt_scalef32_pk_f32_fp4 v[152:153], v196, 1.0
	v_cvt_scalef32_pk_f32_fp4 v[154:155], v196, 1.0 op_sel:[1,0,0]
	v_cvt_scalef32_pk_f32_fp4 v[156:157], v196, 1.0 op_sel:[0,1,0]
	v_cvt_scalef32_pk_f32_fp4 v[158:159], v196, 1.0 op_sel:[1,1,0]
	v_cvt_scalef32_pk_f32_fp4 v[160:161], v197, 1.0
	v_pk_fma_f32 v[120:121], v[230:231], v[152:153], v[120:121] op_sel:[1,0,0] op_sel_hi:[1,1,1]
	v_cvt_scalef32_pk_f32_fp4 v[162:163], v197, 1.0 op_sel:[1,0,0]
	v_pk_fma_f32 v[122:123], v[230:231], v[154:155], v[122:123] op_sel:[1,0,0] op_sel_hi:[1,1,1]
	v_cvt_scalef32_pk_f32_fp4 v[152:153], v197, 1.0 op_sel:[0,1,0]
	v_pk_fma_f32 v[124:125], v[230:231], v[156:157], v[124:125] op_sel:[1,0,0] op_sel_hi:[1,1,1]
	v_cvt_scalef32_pk_f32_fp4 v[154:155], v197, 1.0 op_sel:[1,1,0]
	v_pk_fma_f32 v[126:127], v[230:231], v[158:159], v[126:127] op_sel:[1,0,0] op_sel_hi:[1,1,1]
	v_cvt_scalef32_pk_f32_fp4 v[156:157], v198, 1.0
	v_pk_fma_f32 v[128:129], v[230:231], v[160:161], v[128:129] op_sel:[1,0,0] op_sel_hi:[1,1,1]
; __device__ void phase_exp_v(KParams& p, char* smem) {
;     ...
;         {
;           float* red = reinterpret_cast<float*>(smem + 8192) + w * 2304;
;           float* mr = red + (sub * 8 + cc) * 36;
; #pragma unroll
;           for (int q4 = 0; q4 < 8; ++q4)
;             *reinterpret_cast<float4*>(mr + q4 * 4) = float4{acc[q4 * 2].x, acc[q4 * 2].y, acc[q4 * 2 + 1].x, acc[q4 * 2 + 1].y};
;           __builtin_amdgcn_wave_barrier();
;           float4 r = *reinterpret_cast<const float4*>(red + (0 * 8 + sub) * 36 + cc * 4);
; #pragma unroll
;           for (int s8 = 1; s8 < 8; ++s8) {
;             const float4 r1 = *reinterpret_cast<const float4*>(red + (s8 * 8 + sub) * 36 + cc * 4);
;             r.x += r1.x; r.y += r1.y; r.z += r1.z; r.w += r1.w;
;           }
;           uint2 o4;
;           o4.x = pack2(r.x, r.y);
;           o4.y = pack2(r.z, r.w);
;           *reinterpret_cast<uint2*>(yfb + (size_t)t * D + x * 256 + sub * 32 + cc * 4) = o4;
;           __builtin_amdgcn_wave_barrier();
;         }
;       }
	v_cvt_scalef32_pk_f32_fp4 v[158:159], v198, 1.0 op_sel:[1,0,0]
	v_pk_fma_f32 v[130:131], v[230:231], v[162:163], v[130:131] op_sel:[1,0,0] op_sel_hi:[1,1,1]
	v_cvt_scalef32_pk_f32_fp4 v[160:161], v198, 1.0 op_sel:[0,1,0]
	v_pk_fma_f32 v[132:133], v[230:231], v[152:153], v[132:133] op_sel:[1,0,0] op_sel_hi:[1,1,1]
	v_cvt_scalef32_pk_f32_fp4 v[162:163], v198, 1.0 op_sel:[1,1,0]
	v_pk_fma_f32 v[134:135], v[230:231], v[154:155], v[134:135] op_sel:[1,0,0] op_sel_hi:[1,1,1]
	v_cvt_scalef32_pk_f32_fp4 v[152:153], v199, 1.0
	v_pk_fma_f32 v[136:137], v[230:231], v[156:157], v[136:137] op_sel:[1,0,0] op_sel_hi:[1,1,1]
	v_cvt_scalef32_pk_f32_fp4 v[154:155], v199, 1.0 op_sel:[1,0,0]
	v_pk_fma_f32 v[138:139], v[230:231], v[158:159], v[138:139] op_sel:[1,0,0] op_sel_hi:[1,1,1]
	v_cvt_scalef32_pk_f32_fp4 v[156:157], v199, 1.0 op_sel:[0,1,0]
	v_pk_fma_f32 v[140:141], v[230:231], v[160:161], v[140:141] op_sel:[1,0,0] op_sel_hi:[1,1,1]
	v_cvt_scalef32_pk_f32_fp4 v[158:159], v199, 1.0 op_sel:[1,1,0]
	v_pk_fma_f32 v[142:143], v[230:231], v[162:163], v[142:143] op_sel:[1,0,0] op_sel_hi:[1,1,1]
	v_pk_fma_f32 v[144:145], v[230:231], v[152:153], v[144:145] op_sel:[1,0,0] op_sel_hi:[1,1,1]
	v_pk_fma_f32 v[146:147], v[230:231], v[154:155], v[146:147] op_sel:[1,0,0] op_sel_hi:[1,1,1]
	v_pk_fma_f32 v[148:149], v[230:231], v[156:157], v[148:149] op_sel:[1,0,0] op_sel_hi:[1,1,1]
	v_pk_fma_f32 v[150:151], v[230:231], v[158:159], v[150:151] op_sel:[1,0,0] op_sel_hi:[1,1,1]
	v_and_b32_e32 v170, 8, v44
	s_nop 0
	v_permlane32_swap_b32_e32 v120, v136
	v_permlane32_swap_b32_e32 v121, v137
	v_permlane32_swap_b32_e32 v122, v138
	v_permlane32_swap_b32_e32 v123, v139
	v_permlane32_swap_b32_e32 v124, v140
	v_permlane32_swap_b32_e32 v125, v141
	v_permlane32_swap_b32_e32 v126, v142
	v_permlane32_swap_b32_e32 v127, v143
	v_permlane32_swap_b32_e32 v128, v144
	v_permlane32_swap_b32_e32 v129, v145
	v_permlane32_swap_b32_e32 v130, v146
	v_permlane32_swap_b32_e32 v131, v147
	v_permlane32_swap_b32_e32 v132, v148
	v_permlane32_swap_b32_e32 v133, v149
	v_permlane32_swap_b32_e32 v134, v150
	v_permlane32_swap_b32_e32 v135, v151
	v_pk_add_f32 v[120:121], v[120:121], v[136:137]
	v_pk_add_f32 v[122:123], v[122:123], v[138:139]
	v_pk_add_f32 v[124:125], v[124:125], v[140:141]
	v_pk_add_f32 v[126:127], v[126:127], v[142:143]
	v_pk_add_f32 v[128:129], v[128:129], v[144:145]
	v_pk_add_f32 v[130:131], v[130:131], v[146:147]
	v_pk_add_f32 v[132:133], v[132:133], v[148:149]
	v_pk_add_f32 v[134:135], v[134:135], v[150:151]
	v_cmp_ne_u32_e32 vcc, 0, v170
	s_nop 0
	v_permlane16_swap_b32_e32 v120, v128
	v_permlane16_swap_b32_e32 v121, v129
	v_permlane16_swap_b32_e32 v122, v130
	v_permlane16_swap_b32_e32 v123, v131
	v_permlane16_swap_b32_e32 v124, v132
	v_permlane16_swap_b32_e32 v125, v133
	v_permlane16_swap_b32_e32 v126, v134
	v_permlane16_swap_b32_e32 v127, v135
	v_pk_add_f32 v[120:121], v[120:121], v[128:129]
	v_pk_add_f32 v[122:123], v[122:123], v[130:131]
	v_pk_add_f32 v[124:125], v[124:125], v[132:133]
	v_pk_add_f32 v[126:127], v[126:127], v[134:135]
	s_nop 1
	v_add_f32_dpp v136, v120, v120 row_ror:8 row_mask:0xf bank_mask:0xf
	v_add_f32_dpp v137, v121, v121 row_ror:8 row_mask:0xf bank_mask:0xf
	v_add_f32_dpp v138, v122, v122 row_ror:8 row_mask:0xf bank_mask:0xf
	v_add_f32_dpp v139, v123, v123 row_ror:8 row_mask:0xf bank_mask:0xf
	v_add_f32_dpp v140, v124, v124 row_ror:8 row_mask:0xf bank_mask:0xf
	v_add_f32_dpp v141, v125, v125 row_ror:8 row_mask:0xf bank_mask:0xf
	v_add_f32_dpp v142, v126, v126 row_ror:8 row_mask:0xf bank_mask:0xf
	v_add_f32_dpp v143, v127, v127 row_ror:8 row_mask:0xf bank_mask:0xf
	v_cndmask_b32_e32 v136, v136, v140, vcc
	v_cndmask_b32_e32 v137, v137, v141, vcc
	v_cndmask_b32_e32 v138, v138, v142, vcc
	v_cndmask_b32_e32 v139, v139, v143, vcc
	v_cvt_pk_bf16_f32 v176, v136, v137
	v_cvt_pk_bf16_f32 v177, v138, v139
	v_lshl_add_u64 v[118:119], v[52:53], 0, s[18:19]
	s_add_u32 s18, s18, 0x1000
	v_add_co_u32_e32 v118, vcc, s14, v118
	s_addc_u32 s19, s19, 0
	s_nop 0
	v_addc_co_u32_e32 v119, vcc, 0, v119, vcc
	global_store_dwordx2 v[118:119], v[176:177], off
	s_cmp_eq_u32 s18, 0x10000
	s_cbranch_scc0 .LBB0_1393
	s_branch .LBB0_1381
